# P1 epilogue stores sc0 sc1 as well
# baseline (speedup 1.0000x reference)
.LBB2_50:
	s_mul_i32 s0, s65, 0xc00
	v_cvt_f32_i32_e32 v149, v125
	v_cvt_f32_i32_e32 v148, v124
	v_cvt_f32_i32_e32 v151, v127
	v_cvt_f32_i32_e32 v150, v126
	s_add_i32 s0, s0, 0
	s_add_i32 s4, s0, 0x20000
	v_lshl_or_b32 v144, s64, 8, v202
	v_lshl_add_u32 v146, s23, 8, v201
	s_mov_b64 s[0:1], -1
	s_and_b64 vcc, exec, s[30:31]
	v_ashrrev_i32_e32 v145, 31, v144
	v_lshl_add_u32 v163, v202, 2, s4
	v_lshl_add_u32 v162, v201, 2, s4
	s_cbranch_vccz .LBB2_86
	ds_read2st64_b32 v[152:153], v162 offset1:4
	ds_read_b128 v[136:139], v163 offset:2048
	ds_read_b128 v[132:135], v163 offset:2064
	ds_read_b128 v[128:131], v163 offset:2080
	ds_read_b128 v[124:127], v163 offset:2096
	s_waitcnt lgkmcnt(4)
	v_mov_b32_e32 v154, v153
	v_mov_b32_e32 v153, v152
	v_mov_b32_e32 v155, v154
	s_waitcnt lgkmcnt(3)
	v_pk_mul_f32 v[140:141], v[138:139], v[150:151]
	v_pk_mul_f32 v[142:143], v[136:137], v[148:149]
	s_cmp_gt_i32 s23, 7
	v_pk_fma_f32 v[156:157], v[142:143], v[152:153], v[154:155] op_sel_hi:[1,0,0]
	v_pk_fma_f32 v[158:159], v[140:141], v[152:153], v[154:155] op_sel_hi:[1,0,0]
	s_cbranch_scc0 .LBB2_67
	v_cvt_f32_i32_e32 v141, v121
	v_cvt_f32_i32_e32 v143, v123
	v_cvt_f32_i32_e32 v142, v122
	v_cvt_f32_i32_e32 v140, v120
	v_cvt_f32_i32_e32 v169, v119
	v_cvt_f32_i32_e32 v168, v118
	s_waitcnt lgkmcnt(2)
	v_pk_mul_f32 v[142:143], v[134:135], v[142:143]
	v_pk_mul_f32 v[140:141], v[132:133], v[140:141]
	v_mov_b32_e32 v160, v154
	v_mov_b32_e32 v161, v154
	v_mov_b32_e32 v164, v152
	v_mov_b32_e32 v165, v152
	v_cvt_f32_i32_e32 v167, v117
	v_cvt_f32_i32_e32 v166, v116
	v_pk_fma_f32 v[170:171], v[142:143], v[164:165], v[160:161]
	v_pk_fma_f32 v[142:143], v[140:141], v[152:153], v[154:155]
	s_waitcnt lgkmcnt(1)
	v_pk_mul_f32 v[140:141], v[130:131], v[168:169]
	v_cvt_f32_i32_e32 v173, v113
	v_cvt_f32_i32_e32 v172, v112
	v_pk_fma_f32 v[168:169], v[140:141], v[164:165], v[160:161]
	v_pk_mul_f32 v[166:167], v[128:129], v[166:167]
	v_cvt_pk_fp8_f32 v140, v156, v157
	v_cvt_pk_fp8_f32 v141, v142, v143
	v_cvt_f32_i32_e32 v175, v115
	v_cvt_f32_i32_e32 v174, v114
	s_waitcnt lgkmcnt(0)
	v_pk_mul_f32 v[172:173], v[124:125], v[172:173]
	v_pk_fma_f32 v[166:167], v[166:167], v[152:153], v[154:155]
	v_pk_fma_f32 v[172:173], v[172:173], v[152:153], v[154:155]
	v_cvt_pk_fp8_f32 v140, v158, v159 op_sel:[0,0,1]
	v_cvt_pk_fp8_f32 v142, v166, v167
	v_cvt_pk_fp8_f32 v143, v172, v173
	v_cvt_pk_fp8_f32 v141, v170, v171 op_sel:[0,0,1]
	v_pk_mul_f32 v[174:175], v[126:127], v[174:175]
	v_cvt_pk_fp8_f32 v142, v168, v169 op_sel:[0,0,1]
	v_pk_fma_f32 v[160:161], v[174:175], v[164:165], v[160:161]
	s_mov_b32 s23, s22
	v_cvt_pk_fp8_f32 v143, v160, v161 op_sel:[0,0,1]
	v_mov_b64_e32 v[168:169], s[22:23]
	v_mov_b32_e32 v147, v195
	v_lshlrev_b64 v[160:161], 13, v[146:147]
	v_mfma_f32_16x16x32_fp8_fp8 v[164:167], v[140:141], v[168:169], 0
	v_lshl_add_u64 v[160:161], s[10:11], 0, v[160:161]
	v_lshl_add_u64 v[160:161], v[160:161], 0, v[144:145]
	global_store_dwordx4 v[160:161], v[140:143], off sc0 sc1
	s_nop 1
	v_mfma_f32_16x16x32_fp8_fp8 v[140:143], v[142:143], v[168:169], v[164:167]
	s_and_saveexec_b64 s[0:1], s[20:21]
	s_cbranch_execz .LBB2_54
	s_lshl_b32 s4, s64, 2
	s_or_b32 s4, s4, s46
	s_ashr_i32 s5, s4, 31
	s_lshl_b64 s[4:5], s[4:5], 14
	s_add_u32 s4, s2, s4
	s_addc_u32 s5, s3, s5
	v_lshl_add_u64 v[160:161], v[146:147], 2, s[4:5]
	v_lshlrev_b32_e32 v194, 2, v192
	v_lshl_add_u64 v[160:161], v[160:161], 0, v[194:195]
	global_store_dwordx4 v[160:161], v[140:143], off sc0 sc1
.LBB2_54:
	s_or_b64 exec, exec, s[0:1]
	v_add_u32_e32 v160, 64, v162
	ds_read2st64_b32 v[164:165], v160 offset1:4
	s_nop 2
	v_cvt_f32_i32_e32 v141, v109
	v_cvt_f32_i32_e32 v140, v108
	v_cvt_f32_i32_e32 v171, v107
	v_cvt_f32_i32_e32 v170, v106
	v_cvt_f32_i32_e32 v175, v103
	v_cvt_f32_i32_e32 v174, v102
	v_cvt_f32_i32_e32 v169, v105
	v_cvt_f32_i32_e32 v168, v104
	v_pk_mul_f32 v[140:141], v[136:137], v[140:141]
	s_waitcnt lgkmcnt(0)
	v_mov_b32_e32 v166, v165
	v_pk_fma_f32 v[172:173], v[140:141], v[164:165], v[166:167] op_sel_hi:[1,0,0]
	v_pk_mul_f32 v[140:141], v[134:135], v[170:171]
	v_cvt_f32_i32_e32 v143, v111
	v_cvt_f32_i32_e32 v142, v110
	v_pk_fma_f32 v[176:177], v[140:141], v[164:165], v[166:167] op_sel_hi:[1,0,0]
	v_pk_mul_f32 v[140:141], v[130:131], v[174:175]
	v_pk_mul_f32 v[168:169], v[132:133], v[168:169]
	v_cvt_f32_i32_e32 v171, v101
	v_cvt_f32_i32_e32 v170, v100
	v_pk_fma_f32 v[174:175], v[140:141], v[164:165], v[166:167] op_sel_hi:[1,0,0]
	v_cvt_f32_i32_e32 v179, v93
	v_cvt_f32_i32_e32 v178, v92
	v_pk_fma_f32 v[168:169], v[168:169], v[164:165], v[166:167] op_sel_hi:[1,0,0]
	v_cvt_pk_fp8_f32 v140, v172, v173
	v_pk_mul_f32 v[142:143], v[138:139], v[142:143]
	v_cvt_pk_fp8_f32 v141, v168, v169
	v_pk_fma_f32 v[142:143], v[142:143], v[164:165], v[166:167] op_sel_hi:[1,0,0]
	v_pk_mul_f32 v[170:171], v[128:129], v[170:171]
	v_cvt_f32_i32_e32 v181, v95
	v_cvt_f32_i32_e32 v180, v94
	v_pk_mul_f32 v[168:169], v[124:125], v[178:179]
	v_pk_fma_f32 v[170:171], v[170:171], v[164:165], v[166:167] op_sel_hi:[1,0,0]
	v_pk_fma_f32 v[168:169], v[168:169], v[164:165], v[166:167] op_sel_hi:[1,0,0]
	v_cvt_pk_fp8_f32 v140, v142, v143 op_sel:[0,0,1]
	v_cvt_pk_fp8_f32 v141, v176, v177 op_sel:[0,0,1]
	v_cvt_pk_fp8_f32 v142, v170, v171
	v_cvt_pk_fp8_f32 v143, v168, v169
	v_pk_mul_f32 v[168:169], v[126:127], v[180:181]
	v_mov_b64_e32 v[170:171], s[22:23]
	v_pk_fma_f32 v[164:165], v[168:169], v[164:165], v[166:167] op_sel_hi:[1,0,0]
	v_cvt_pk_fp8_f32 v142, v174, v175 op_sel:[0,0,1]
	v_cvt_pk_fp8_f32 v143, v164, v165 op_sel:[0,0,1]
	v_or_b32_e32 v194, 16, v146
	v_mfma_f32_16x16x32_fp8_fp8 v[164:167], v[140:141], v[170:171], 0
	v_lshlrev_b64 v[168:169], 13, v[194:195]
	v_lshl_add_u64 v[168:169], s[10:11], 0, v[168:169]
	v_lshl_add_u64 v[168:169], v[168:169], 0, v[144:145]
	global_store_dwordx4 v[168:169], v[140:143], off sc0 sc1
	s_nop 1
	v_mfma_f32_16x16x32_fp8_fp8 v[140:143], v[142:143], v[170:171], v[164:167]
	s_and_saveexec_b64 s[0:1], s[20:21]
	s_cbranch_execz .LBB2_56
	s_lshl_b32 s4, s64, 2
	s_or_b32 s4, s4, s46
	s_ashr_i32 s5, s4, 31
	s_lshl_b64 s[4:5], s[4:5], 14
	s_add_u32 s4, s2, s4
	s_addc_u32 s5, s3, s5
	v_lshl_add_u64 v[164:165], v[146:147], 2, s[4:5]
	v_lshlrev_b32_e32 v194, 2, v192
	v_lshl_add_u64 v[164:165], v[164:165], 0, v[194:195]
	global_store_dwordx4 v[164:165], v[140:143], off offset:64 sc0 sc1
.LBB2_56:
	s_or_b64 exec, exec, s[0:1]
	v_add_u32_e32 v161, 0x80, v162
	ds_read2st64_b32 v[164:165], v161 offset1:4
	s_nop 2
	v_cvt_f32_i32_e32 v141, v97
	v_cvt_f32_i32_e32 v140, v96
	v_cvt_f32_i32_e32 v171, v91
	v_cvt_f32_i32_e32 v170, v90
	v_cvt_f32_i32_e32 v175, v87
	v_cvt_f32_i32_e32 v174, v86
	v_cvt_f32_i32_e32 v169, v89
	v_cvt_f32_i32_e32 v168, v88
	v_pk_mul_f32 v[140:141], v[136:137], v[140:141]
	s_waitcnt lgkmcnt(0)
	v_mov_b32_e32 v166, v165
	v_pk_fma_f32 v[172:173], v[140:141], v[164:165], v[166:167] op_sel_hi:[1,0,0]
	v_pk_mul_f32 v[140:141], v[134:135], v[170:171]
	v_cvt_f32_i32_e32 v143, v99
	v_cvt_f32_i32_e32 v142, v98
	v_pk_fma_f32 v[176:177], v[140:141], v[164:165], v[166:167] op_sel_hi:[1,0,0]
	v_pk_mul_f32 v[140:141], v[130:131], v[174:175]
	v_pk_mul_f32 v[168:169], v[132:133], v[168:169]
	v_cvt_f32_i32_e32 v171, v85
	v_cvt_f32_i32_e32 v170, v84
	v_pk_fma_f32 v[178:179], v[140:141], v[164:165], v[166:167] op_sel_hi:[1,0,0]
	v_cvt_f32_i32_e32 v181, v77
	v_cvt_f32_i32_e32 v180, v76
	v_pk_fma_f32 v[168:169], v[168:169], v[164:165], v[166:167] op_sel_hi:[1,0,0]
	v_cvt_pk_fp8_f32 v140, v172, v173
	v_pk_mul_f32 v[142:143], v[138:139], v[142:143]
	v_cvt_pk_fp8_f32 v141, v168, v169
	v_pk_fma_f32 v[142:143], v[142:143], v[164:165], v[166:167] op_sel_hi:[1,0,0]
	v_pk_mul_f32 v[170:171], v[128:129], v[170:171]
	v_cvt_f32_i32_e32 v175, v79
	v_cvt_f32_i32_e32 v174, v78
	v_pk_mul_f32 v[168:169], v[124:125], v[180:181]
	v_pk_fma_f32 v[170:171], v[170:171], v[164:165], v[166:167] op_sel_hi:[1,0,0]
	v_pk_fma_f32 v[168:169], v[168:169], v[164:165], v[166:167] op_sel_hi:[1,0,0]
	v_cvt_pk_fp8_f32 v140, v142, v143 op_sel:[0,0,1]
	v_cvt_pk_fp8_f32 v141, v176, v177 op_sel:[0,0,1]
	v_cvt_pk_fp8_f32 v142, v170, v171
	v_cvt_pk_fp8_f32 v143, v168, v169
	v_pk_mul_f32 v[174:175], v[126:127], v[174:175]
	s_mov_b32 s23, s22
	v_pk_fma_f32 v[164:165], v[174:175], v[164:165], v[166:167] op_sel_hi:[1,0,0]
	v_cvt_pk_fp8_f32 v142, v178, v179 op_sel:[0,0,1]
	v_cvt_pk_fp8_f32 v143, v164, v165 op_sel:[0,0,1]
	v_mov_b64_e32 v[170:171], s[22:23]
	v_or_b32_e32 v194, 32, v146
	v_lshlrev_b64 v[168:169], 13, v[194:195]
	v_mfma_f32_16x16x32_fp8_fp8 v[164:167], v[140:141], v[170:171], 0
	v_lshl_add_u64 v[168:169], s[10:11], 0, v[168:169]
	v_lshl_add_u64 v[168:169], v[168:169], 0, v[144:145]
	global_store_dwordx4 v[168:169], v[140:143], off sc0 sc1
	s_nop 1
	v_mfma_f32_16x16x32_fp8_fp8 v[140:143], v[142:143], v[170:171], v[164:167]
	s_and_saveexec_b64 s[0:1], s[20:21]
	s_cbranch_execz .LBB2_58
	s_lshl_b32 s4, s64, 2
	s_or_b32 s4, s4, s46
	s_ashr_i32 s5, s4, 31
	s_lshl_b64 s[4:5], s[4:5], 14
	s_add_u32 s4, s2, s4
	s_addc_u32 s5, s3, s5
	v_lshl_add_u64 v[164:165], v[146:147], 2, s[4:5]
	v_lshlrev_b32_e32 v194, 2, v192
	v_lshl_add_u64 v[164:165], v[164:165], 0, v[194:195]
	global_store_dwordx4 v[164:165], v[140:143], off offset:128 sc0 sc1
.LBB2_58:
	s_or_b64 exec, exec, s[0:1]
	v_add_u32_e32 v164, 0xc0, v162
	ds_read2st64_b32 v[166:167], v164 offset1:4
	s_nop 2
	v_cvt_f32_i32_e32 v141, v81
	v_cvt_f32_i32_e32 v140, v80
	v_cvt_f32_i32_e32 v173, v75
	v_cvt_f32_i32_e32 v172, v74
	v_cvt_f32_i32_e32 v177, v71
	v_cvt_f32_i32_e32 v176, v70
	v_cvt_f32_i32_e32 v171, v73
	v_cvt_f32_i32_e32 v170, v72
	v_pk_mul_f32 v[140:141], v[136:137], v[140:141]
	s_waitcnt lgkmcnt(0)
	v_mov_b32_e32 v168, v167
	v_pk_fma_f32 v[174:175], v[140:141], v[166:167], v[168:169] op_sel_hi:[1,0,0]
	v_pk_mul_f32 v[140:141], v[134:135], v[172:173]
	v_cvt_f32_i32_e32 v143, v83
	v_cvt_f32_i32_e32 v142, v82
	v_pk_fma_f32 v[178:179], v[140:141], v[166:167], v[168:169] op_sel_hi:[1,0,0]
	v_pk_mul_f32 v[140:141], v[130:131], v[176:177]
	v_pk_mul_f32 v[170:171], v[132:133], v[170:171]
	v_cvt_f32_i32_e32 v173, v69
	v_cvt_f32_i32_e32 v172, v68
	v_pk_fma_f32 v[176:177], v[140:141], v[166:167], v[168:169] op_sel_hi:[1,0,0]
	v_cvt_f32_i32_e32 v181, v65
	v_cvt_f32_i32_e32 v180, v64
	v_pk_fma_f32 v[170:171], v[170:171], v[166:167], v[168:169] op_sel_hi:[1,0,0]
	v_cvt_pk_fp8_f32 v140, v174, v175
	v_pk_mul_f32 v[142:143], v[138:139], v[142:143]
	v_cvt_pk_fp8_f32 v141, v170, v171
	v_pk_fma_f32 v[142:143], v[142:143], v[166:167], v[168:169] op_sel_hi:[1,0,0]
	v_pk_mul_f32 v[172:173], v[128:129], v[172:173]
	v_cvt_f32_i32_e32 v183, v67
	v_cvt_f32_i32_e32 v182, v66
	v_pk_mul_f32 v[170:171], v[124:125], v[180:181]
	v_pk_fma_f32 v[172:173], v[172:173], v[166:167], v[168:169] op_sel_hi:[1,0,0]
	v_pk_fma_f32 v[170:171], v[170:171], v[166:167], v[168:169] op_sel_hi:[1,0,0]
	v_cvt_pk_fp8_f32 v140, v142, v143 op_sel:[0,0,1]
	v_cvt_pk_fp8_f32 v141, v178, v179 op_sel:[0,0,1]
	v_cvt_pk_fp8_f32 v142, v172, v173
	v_cvt_pk_fp8_f32 v143, v170, v171
	v_pk_mul_f32 v[170:171], v[126:127], v[182:183]
	v_mov_b64_e32 v[172:173], s[22:23]
	v_pk_fma_f32 v[166:167], v[170:171], v[166:167], v[168:169] op_sel_hi:[1,0,0]
	v_cvt_pk_fp8_f32 v142, v176, v177 op_sel:[0,0,1]
	v_cvt_pk_fp8_f32 v143, v166, v167 op_sel:[0,0,1]
	v_or_b32_e32 v194, 48, v146
	v_mfma_f32_16x16x32_fp8_fp8 v[166:169], v[140:141], v[172:173], 0
	v_lshlrev_b64 v[170:171], 13, v[194:195]
	v_lshl_add_u64 v[170:171], s[10:11], 0, v[170:171]
	v_lshl_add_u64 v[170:171], v[170:171], 0, v[144:145]
	global_store_dwordx4 v[170:171], v[140:143], off sc0 sc1
	s_nop 1
	v_mfma_f32_16x16x32_fp8_fp8 v[140:143], v[142:143], v[172:173], v[166:169]
	s_and_saveexec_b64 s[0:1], s[20:21]
	s_cbranch_execz .LBB2_60
	s_lshl_b32 s4, s64, 2
	s_or_b32 s4, s4, s46
	s_ashr_i32 s5, s4, 31
	s_lshl_b64 s[4:5], s[4:5], 14
	s_add_u32 s4, s2, s4
	s_addc_u32 s5, s3, s5
	v_lshl_add_u64 v[166:167], v[146:147], 2, s[4:5]
	v_lshlrev_b32_e32 v194, 2, v192
	v_lshl_add_u64 v[166:167], v[166:167], 0, v[194:195]
	global_store_dwordx4 v[166:167], v[140:143], off offset:192 sc0 sc1
.LBB2_60:
	s_or_b64 exec, exec, s[0:1]
	ds_read2st64_b32 v[166:167], v162 offset0:2 offset1:6
	s_nop 3
	v_cvt_f32_i32_e32 v141, v61
	v_cvt_f32_i32_e32 v140, v60
	v_cvt_f32_i32_e32 v173, v59
	v_cvt_f32_i32_e32 v172, v58
	v_cvt_f32_i32_e32 v177, v51
	v_cvt_f32_i32_e32 v176, v50
	v_cvt_f32_i32_e32 v171, v57
	v_cvt_f32_i32_e32 v170, v56
	v_pk_mul_f32 v[140:141], v[136:137], v[140:141]
	s_waitcnt lgkmcnt(0)
	v_mov_b32_e32 v168, v167
	v_pk_fma_f32 v[174:175], v[140:141], v[166:167], v[168:169] op_sel_hi:[1,0,0]
	v_pk_mul_f32 v[140:141], v[134:135], v[172:173]
	v_cvt_f32_i32_e32 v143, v63
	v_cvt_f32_i32_e32 v142, v62
	v_pk_fma_f32 v[178:179], v[140:141], v[166:167], v[168:169] op_sel_hi:[1,0,0]
	v_pk_mul_f32 v[140:141], v[130:131], v[176:177]
	v_pk_mul_f32 v[170:171], v[132:133], v[170:171]
	v_cvt_f32_i32_e32 v173, v49
	v_cvt_f32_i32_e32 v172, v48
	v_pk_fma_f32 v[176:177], v[140:141], v[166:167], v[168:169] op_sel_hi:[1,0,0]
	v_cvt_f32_i32_e32 v181, v41
	v_cvt_f32_i32_e32 v180, v40
	v_pk_fma_f32 v[170:171], v[170:171], v[166:167], v[168:169] op_sel_hi:[1,0,0]
	v_cvt_pk_fp8_f32 v140, v174, v175
	v_pk_mul_f32 v[142:143], v[138:139], v[142:143]
	v_cvt_pk_fp8_f32 v141, v170, v171
	v_pk_fma_f32 v[142:143], v[142:143], v[166:167], v[168:169] op_sel_hi:[1,0,0]
	v_pk_mul_f32 v[172:173], v[128:129], v[172:173]
	v_cvt_f32_i32_e32 v183, v43
	v_cvt_f32_i32_e32 v182, v42
	v_pk_mul_f32 v[170:171], v[124:125], v[180:181]
	v_pk_fma_f32 v[172:173], v[172:173], v[166:167], v[168:169] op_sel_hi:[1,0,0]
	v_pk_fma_f32 v[170:171], v[170:171], v[166:167], v[168:169] op_sel_hi:[1,0,0]
	v_cvt_pk_fp8_f32 v140, v142, v143 op_sel:[0,0,1]
	v_cvt_pk_fp8_f32 v141, v178, v179 op_sel:[0,0,1]
	v_cvt_pk_fp8_f32 v142, v172, v173
	v_cvt_pk_fp8_f32 v143, v170, v171
	v_pk_mul_f32 v[170:171], v[126:127], v[182:183]
	s_mov_b32 s23, s22
	v_pk_fma_f32 v[166:167], v[170:171], v[166:167], v[168:169] op_sel_hi:[1,0,0]
	v_cvt_pk_fp8_f32 v142, v176, v177 op_sel:[0,0,1]
	v_cvt_pk_fp8_f32 v143, v166, v167 op_sel:[0,0,1]
	v_mov_b64_e32 v[172:173], s[22:23]
	v_add_u32_e32 v194, 0x80, v146
	v_lshlrev_b64 v[170:171], 13, v[194:195]
	v_mfma_f32_16x16x32_fp8_fp8 v[166:169], v[140:141], v[172:173], 0
	v_lshl_add_u64 v[170:171], s[10:11], 0, v[170:171]
	v_lshl_add_u64 v[170:171], v[170:171], 0, v[144:145]
	global_store_dwordx4 v[170:171], v[140:143], off sc0 sc1
	s_nop 1
	v_mfma_f32_16x16x32_fp8_fp8 v[140:143], v[142:143], v[172:173], v[166:169]
	s_and_saveexec_b64 s[0:1], s[20:21]
	s_cbranch_execz .LBB2_62
	s_lshl_b32 s4, s64, 2
	s_or_b32 s4, s4, s46
	s_ashr_i32 s5, s4, 31
	s_lshl_b64 s[4:5], s[4:5], 14
	s_add_u32 s4, s2, s4
	s_addc_u32 s5, s3, s5
	v_lshl_add_u64 v[166:167], v[146:147], 2, s[4:5]
	v_lshlrev_b32_e32 v194, 2, v192
	v_lshl_add_u64 v[166:167], v[166:167], 0, v[194:195]
	global_store_dwordx4 v[166:167], v[140:143], off offset:512 sc0 sc1
.LBB2_62:
	s_or_b64 exec, exec, s[0:1]
	ds_read2st64_b32 v[166:167], v160 offset0:2 offset1:6
	s_nop 3
	v_cvt_f32_i32_e32 v141, v53
	v_cvt_f32_i32_e32 v140, v52
	v_cvt_f32_i32_e32 v171, v47
	v_cvt_f32_i32_e32 v170, v46
	v_cvt_f32_i32_e32 v175, v35
	v_cvt_f32_i32_e32 v174, v34
	v_cvt_f32_i32_e32 v169, v45
	v_cvt_f32_i32_e32 v168, v44
	v_pk_mul_f32 v[140:141], v[136:137], v[140:141]
	s_waitcnt lgkmcnt(0)
	v_mov_b32_e32 v160, v167
	v_pk_fma_f32 v[172:173], v[140:141], v[166:167], v[160:161] op_sel_hi:[1,0,0]
	v_pk_mul_f32 v[140:141], v[134:135], v[170:171]
	v_cvt_f32_i32_e32 v143, v55
	v_cvt_f32_i32_e32 v142, v54
	v_pk_fma_f32 v[176:177], v[140:141], v[166:167], v[160:161] op_sel_hi:[1,0,0]
	v_pk_mul_f32 v[140:141], v[130:131], v[174:175]
	v_pk_mul_f32 v[168:169], v[132:133], v[168:169]
	v_cvt_f32_i32_e32 v171, v33
	v_cvt_f32_i32_e32 v170, v32
	v_pk_fma_f32 v[174:175], v[140:141], v[166:167], v[160:161] op_sel_hi:[1,0,0]
	v_cvt_f32_i32_e32 v179, v25
	v_cvt_f32_i32_e32 v178, v24
	v_pk_fma_f32 v[168:169], v[168:169], v[166:167], v[160:161] op_sel_hi:[1,0,0]
	v_cvt_pk_fp8_f32 v140, v172, v173
	v_pk_mul_f32 v[142:143], v[138:139], v[142:143]
	v_cvt_pk_fp8_f32 v141, v168, v169
	v_pk_fma_f32 v[142:143], v[142:143], v[166:167], v[160:161] op_sel_hi:[1,0,0]
	v_pk_mul_f32 v[170:171], v[128:129], v[170:171]
	v_cvt_f32_i32_e32 v181, v27
	v_cvt_f32_i32_e32 v180, v26
	v_pk_mul_f32 v[168:169], v[124:125], v[178:179]
	v_pk_fma_f32 v[170:171], v[170:171], v[166:167], v[160:161] op_sel_hi:[1,0,0]
	v_pk_fma_f32 v[168:169], v[168:169], v[166:167], v[160:161] op_sel_hi:[1,0,0]
	v_cvt_pk_fp8_f32 v140, v142, v143 op_sel:[0,0,1]
	v_cvt_pk_fp8_f32 v141, v176, v177 op_sel:[0,0,1]
	v_cvt_pk_fp8_f32 v142, v170, v171
	v_cvt_pk_fp8_f32 v143, v168, v169
	v_pk_mul_f32 v[168:169], v[126:127], v[180:181]
	v_mov_b64_e32 v[172:173], s[22:23]
	v_pk_fma_f32 v[166:167], v[168:169], v[166:167], v[160:161] op_sel_hi:[1,0,0]
	v_cvt_pk_fp8_f32 v142, v174, v175 op_sel:[0,0,1]
	v_cvt_pk_fp8_f32 v143, v166, v167 op_sel:[0,0,1]
	v_add_u32_e32 v194, 0x90, v146
	v_mfma_f32_16x16x32_fp8_fp8 v[166:169], v[140:141], v[172:173], 0
	v_lshlrev_b64 v[170:171], 13, v[194:195]
	v_lshl_add_u64 v[170:171], s[10:11], 0, v[170:171]
	v_lshl_add_u64 v[170:171], v[170:171], 0, v[144:145]
	global_store_dwordx4 v[170:171], v[140:143], off sc0 sc1
	s_nop 1
	v_mfma_f32_16x16x32_fp8_fp8 v[140:143], v[142:143], v[172:173], v[166:169]
	s_and_saveexec_b64 s[0:1], s[20:21]
	s_cbranch_execz .LBB2_64
	s_lshl_b32 s4, s64, 2
	s_or_b32 s4, s4, s46
	s_ashr_i32 s5, s4, 31
	s_lshl_b64 s[4:5], s[4:5], 14
	s_add_u32 s4, s2, s4
	s_addc_u32 s5, s3, s5
	v_lshl_add_u64 v[166:167], v[146:147], 2, s[4:5]
	v_lshlrev_b32_e32 v194, 2, v192
	v_lshl_add_u64 v[166:167], v[166:167], 0, v[194:195]
	global_store_dwordx4 v[166:167], v[140:143], off offset:576 sc0 sc1
.LBB2_64:
	s_or_b64 exec, exec, s[0:1]
	ds_read2st64_b32 v[160:161], v161 offset0:2 offset1:6
	s_nop 3
	v_cvt_f32_i32_e32 v141, v37
	v_cvt_f32_i32_e32 v140, v36
	v_cvt_f32_i32_e32 v171, v31
	v_cvt_f32_i32_e32 v170, v30
	v_cvt_f32_i32_e32 v175, v19
	v_cvt_f32_i32_e32 v174, v18
	v_cvt_f32_i32_e32 v169, v29
	v_cvt_f32_i32_e32 v168, v28
	v_pk_mul_f32 v[140:141], v[136:137], v[140:141]
	s_waitcnt lgkmcnt(0)
	v_mov_b32_e32 v166, v161
	v_pk_fma_f32 v[172:173], v[140:141], v[160:161], v[166:167] op_sel_hi:[1,0,0]
	v_pk_mul_f32 v[140:141], v[134:135], v[170:171]
	v_cvt_f32_i32_e32 v143, v39
	v_cvt_f32_i32_e32 v142, v38
	v_pk_fma_f32 v[176:177], v[140:141], v[160:161], v[166:167] op_sel_hi:[1,0,0]
	v_pk_mul_f32 v[140:141], v[130:131], v[174:175]
	v_pk_mul_f32 v[168:169], v[132:133], v[168:169]
	v_cvt_f32_i32_e32 v171, v17
	v_cvt_f32_i32_e32 v170, v16
	v_pk_fma_f32 v[178:179], v[140:141], v[160:161], v[166:167] op_sel_hi:[1,0,0]
	v_cvt_f32_i32_e32 v181, v9
	v_cvt_f32_i32_e32 v180, v8
	v_pk_fma_f32 v[168:169], v[168:169], v[160:161], v[166:167] op_sel_hi:[1,0,0]
	v_cvt_pk_fp8_f32 v140, v172, v173
	v_pk_mul_f32 v[142:143], v[138:139], v[142:143]
	v_cvt_pk_fp8_f32 v141, v168, v169
	v_pk_fma_f32 v[142:143], v[142:143], v[160:161], v[166:167] op_sel_hi:[1,0,0]
	v_pk_mul_f32 v[170:171], v[128:129], v[170:171]
	v_cvt_f32_i32_e32 v175, v11
	v_cvt_f32_i32_e32 v174, v10
	v_pk_mul_f32 v[168:169], v[124:125], v[180:181]
	v_pk_fma_f32 v[170:171], v[170:171], v[160:161], v[166:167] op_sel_hi:[1,0,0]
	v_pk_fma_f32 v[168:169], v[168:169], v[160:161], v[166:167] op_sel_hi:[1,0,0]
	v_cvt_pk_fp8_f32 v140, v142, v143 op_sel:[0,0,1]
	v_cvt_pk_fp8_f32 v141, v176, v177 op_sel:[0,0,1]
	v_cvt_pk_fp8_f32 v142, v170, v171
	v_cvt_pk_fp8_f32 v143, v168, v169
	v_pk_mul_f32 v[174:175], v[126:127], v[174:175]
	s_mov_b32 s23, s22
	v_pk_fma_f32 v[160:161], v[174:175], v[160:161], v[166:167] op_sel_hi:[1,0,0]
	v_cvt_pk_fp8_f32 v142, v178, v179 op_sel:[0,0,1]
	v_cvt_pk_fp8_f32 v143, v160, v161 op_sel:[0,0,1]
	v_mov_b64_e32 v[170:171], s[22:23]
	v_add_u32_e32 v194, 0xa0, v146
	v_lshlrev_b64 v[160:161], 13, v[194:195]
	v_mfma_f32_16x16x32_fp8_fp8 v[166:169], v[140:141], v[170:171], 0
	v_lshl_add_u64 v[160:161], s[10:11], 0, v[160:161]
	v_lshl_add_u64 v[160:161], v[160:161], 0, v[144:145]
	global_store_dwordx4 v[160:161], v[140:143], off sc0 sc1
	s_nop 1
	v_mfma_f32_16x16x32_fp8_fp8 v[140:143], v[142:143], v[170:171], v[166:169]
	s_and_saveexec_b64 s[0:1], s[20:21]
	s_cbranch_execz .LBB2_66
	s_lshl_b32 s4, s64, 2
	s_or_b32 s4, s4, s46
	s_ashr_i32 s5, s4, 31
	s_lshl_b64 s[4:5], s[4:5], 14
	s_add_u32 s4, s2, s4
	s_addc_u32 s5, s3, s5
	v_lshl_add_u64 v[160:161], v[146:147], 2, s[4:5]
	v_lshlrev_b32_e32 v194, 2, v192
	v_lshl_add_u64 v[160:161], v[160:161], 0, v[194:195]
	global_store_dwordx4 v[160:161], v[140:143], off offset:640 sc0 sc1
.LBB2_66:
	s_or_b64 exec, exec, s[0:1]
	ds_read2st64_b32 v[160:161], v164 offset0:2 offset1:6
	s_nop 3
	v_cvt_f32_i32_e32 v141, v21
	v_cvt_f32_i32_e32 v140, v20
	v_cvt_f32_i32_e32 v169, v15
	v_cvt_f32_i32_e32 v168, v14
	v_cvt_f32_i32_e32 v173, v7
	v_cvt_f32_i32_e32 v172, v6
	v_cvt_f32_i32_e32 v167, v13
	v_cvt_f32_i32_e32 v166, v12
	v_pk_mul_f32 v[140:141], v[136:137], v[140:141]
	s_waitcnt lgkmcnt(0)
	v_mov_b32_e32 v164, v161
	v_pk_fma_f32 v[170:171], v[140:141], v[160:161], v[164:165] op_sel_hi:[1,0,0]
	v_pk_mul_f32 v[140:141], v[134:135], v[168:169]
	v_cvt_f32_i32_e32 v143, v23
	v_cvt_f32_i32_e32 v142, v22
	v_pk_fma_f32 v[174:175], v[140:141], v[160:161], v[164:165] op_sel_hi:[1,0,0]
	v_pk_mul_f32 v[140:141], v[130:131], v[172:173]
	v_pk_mul_f32 v[166:167], v[132:133], v[166:167]
	v_cvt_f32_i32_e32 v169, v5
	v_cvt_f32_i32_e32 v168, v4
	v_pk_fma_f32 v[172:173], v[140:141], v[160:161], v[164:165] op_sel_hi:[1,0,0]
	v_cvt_f32_i32_e32 v177, v1
	v_cvt_f32_i32_e32 v176, v0
	v_pk_fma_f32 v[166:167], v[166:167], v[160:161], v[164:165] op_sel_hi:[1,0,0]
	v_cvt_pk_fp8_f32 v140, v170, v171
	v_pk_mul_f32 v[142:143], v[138:139], v[142:143]
	v_cvt_pk_fp8_f32 v141, v166, v167
	v_pk_fma_f32 v[142:143], v[142:143], v[160:161], v[164:165] op_sel_hi:[1,0,0]
	v_pk_mul_f32 v[168:169], v[128:129], v[168:169]
	v_cvt_f32_i32_e32 v179, v3
	v_cvt_f32_i32_e32 v178, v2
	v_pk_mul_f32 v[166:167], v[124:125], v[176:177]
	v_pk_fma_f32 v[168:169], v[168:169], v[160:161], v[164:165] op_sel_hi:[1,0,0]
	v_pk_fma_f32 v[166:167], v[166:167], v[160:161], v[164:165] op_sel_hi:[1,0,0]
	v_cvt_pk_fp8_f32 v140, v142, v143 op_sel:[0,0,1]
	v_cvt_pk_fp8_f32 v141, v174, v175 op_sel:[0,0,1]
	v_cvt_pk_fp8_f32 v142, v168, v169
	v_cvt_pk_fp8_f32 v143, v166, v167
	v_pk_mul_f32 v[166:167], v[126:127], v[178:179]
	v_mov_b64_e32 v[168:169], s[22:23]
	v_pk_fma_f32 v[160:161], v[166:167], v[160:161], v[164:165] op_sel_hi:[1,0,0]
	v_cvt_pk_fp8_f32 v142, v172, v173 op_sel:[0,0,1]
	v_cvt_pk_fp8_f32 v143, v160, v161 op_sel:[0,0,1]
	v_add_u32_e32 v194, 0xb0, v146
	v_mfma_f32_16x16x32_fp8_fp8 v[164:167], v[140:141], v[168:169], 0
	v_lshlrev_b64 v[160:161], 13, v[194:195]
	v_lshl_add_u64 v[160:161], s[10:11], 0, v[160:161]
	v_lshl_add_u64 v[160:161], v[160:161], 0, v[144:145]
	global_store_dwordx4 v[160:161], v[140:143], off sc0 sc1
	s_mov_b64 s[0:1], s[20:21]
	s_nop 0
	v_mfma_f32_16x16x32_fp8_fp8 v[140:143], v[142:143], v[168:169], v[164:167]
	v_mov_b64_e32 v[160:161], v[194:195]
	s_branch .LBB2_83
.LBB2_67:
	s_mov_b64 s[0:1], 0
	s_cbranch_execz .LBB2_83
	v_cvt_f32_i32_e32 v141, v121
	v_cvt_f32_i32_e32 v143, v123
	v_cvt_f32_i32_e32 v142, v122
	v_cvt_f32_i32_e32 v140, v120
	v_cvt_f32_i32_e32 v169, v119
	v_cvt_f32_i32_e32 v168, v118
	s_waitcnt lgkmcnt(2)
	v_pk_mul_f32 v[142:143], v[134:135], v[142:143]
	v_pk_mul_f32 v[140:141], v[132:133], v[140:141]
	v_mov_b32_e32 v160, v154
	v_mov_b32_e32 v161, v154
	v_mov_b32_e32 v164, v152
	v_mov_b32_e32 v165, v152
	v_pk_fma_f32 v[142:143], v[142:143], v[164:165], v[160:161]
	v_pk_fma_f32 v[140:141], v[140:141], v[152:153], v[154:155]
	v_cvt_f32_i32_e32 v167, v117
	v_cvt_f32_i32_e32 v166, v116
	v_pk_mul_f32 v[170:171], v[142:143], v[142:143]
	v_pk_mul_f32 v[142:143], v[140:141], v[140:141]
	s_waitcnt lgkmcnt(1)
	v_pk_mul_f32 v[140:141], v[130:131], v[168:169]
	v_cvt_f32_i32_e32 v169, v113
	v_cvt_f32_i32_e32 v168, v112
	v_pk_fma_f32 v[140:141], v[140:141], v[164:165], v[160:161]
	v_pk_mul_f32 v[156:157], v[156:157], v[156:157]
	v_pk_mul_f32 v[174:175], v[140:141], v[140:141]
	v_pk_mul_f32 v[166:167], v[128:129], v[166:167]
	v_cvt_pk_fp8_f32 v140, v156, v157
	v_cvt_pk_fp8_f32 v141, v142, v143
	v_cvt_f32_i32_e32 v173, v115
	v_cvt_f32_i32_e32 v172, v114
	s_waitcnt lgkmcnt(0)
	v_pk_mul_f32 v[168:169], v[124:125], v[168:169]
	v_pk_fma_f32 v[166:167], v[166:167], v[152:153], v[154:155]
	v_pk_fma_f32 v[152:153], v[168:169], v[152:153], v[154:155]
	v_pk_mul_f32 v[158:159], v[158:159], v[158:159]
	v_pk_mul_f32 v[166:167], v[166:167], v[166:167]
	v_pk_mul_f32 v[152:153], v[152:153], v[152:153]
	v_cvt_pk_fp8_f32 v140, v158, v159 op_sel:[0,0,1]
	v_cvt_pk_fp8_f32 v142, v166, v167
	v_cvt_pk_fp8_f32 v143, v152, v153
	v_cvt_pk_fp8_f32 v141, v170, v171 op_sel:[0,0,1]
	v_pk_mul_f32 v[172:173], v[126:127], v[172:173]
	v_cvt_pk_fp8_f32 v142, v174, v175 op_sel:[0,0,1]
	v_pk_fma_f32 v[156:157], v[172:173], v[164:165], v[160:161]
	s_mov_b32 s23, s22
	v_pk_mul_f32 v[152:153], v[156:157], v[156:157]
	v_mov_b64_e32 v[158:159], s[22:23]
	v_cvt_pk_fp8_f32 v143, v152, v153 op_sel:[0,0,1]
	v_ashrrev_i32_e32 v147, 31, v146
	v_mfma_f32_16x16x32_fp8_fp8 v[152:155], v[140:141], v[158:159], 0
	v_lshlrev_b64 v[156:157], 13, v[146:147]
	v_lshl_add_u64 v[156:157], s[10:11], 0, v[156:157]
	v_lshl_add_u64 v[156:157], v[156:157], 0, v[144:145]
	global_store_dwordx4 v[156:157], v[140:143], off sc0 sc1
	s_nop 1
	v_mfma_f32_16x16x32_fp8_fp8 v[140:143], v[142:143], v[158:159], v[152:155]
	s_and_saveexec_b64 s[0:1], s[20:21]
	s_cbranch_execz .LBB2_70
	s_lshl_b32 s4, s64, 2
	s_or_b32 s4, s4, s46
	s_ashr_i32 s5, s4, 31
	s_lshl_b64 s[4:5], s[4:5], 14
	s_add_u32 s4, s2, s4
	s_addc_u32 s5, s3, s5
	v_lshl_add_u64 v[152:153], v[146:147], 2, s[4:5]
	v_lshlrev_b32_e32 v194, 2, v192
	v_lshl_add_u64 v[152:153], v[152:153], 0, v[194:195]
	global_store_dwordx4 v[152:153], v[140:143], off sc0 sc1
.LBB2_70:
	s_or_b64 exec, exec, s[0:1]
	v_add_u32_e32 v154, 64, v162
	s_nop 3
	ds_read2st64_b32 v[142:143], v154 offset1:4
	v_cvt_f32_i32_e32 v141, v109
	v_cvt_f32_i32_e32 v140, v108
	v_cvt_f32_i32_e32 v161, v107
	v_cvt_f32_i32_e32 v160, v106
	s_waitcnt lgkmcnt(0)
	v_mov_b32_e32 v156, v143
	v_pk_mul_f32 v[140:141], v[136:137], v[140:141]
	v_cvt_f32_i32_e32 v167, v103
	v_cvt_f32_i32_e32 v166, v102
	v_pk_fma_f32 v[140:141], v[140:141], v[142:143], v[156:157] op_sel_hi:[1,0,0]
	v_cvt_f32_i32_e32 v159, v105
	v_pk_mul_f32 v[164:165], v[140:141], v[140:141]
	v_pk_mul_f32 v[140:141], v[134:135], v[160:161]
	v_cvt_f32_i32_e32 v158, v104
	v_pk_fma_f32 v[140:141], v[140:141], v[142:143], v[156:157] op_sel_hi:[1,0,0]
	v_cvt_f32_i32_e32 v153, v111
	v_pk_mul_f32 v[168:169], v[140:141], v[140:141]
	v_pk_mul_f32 v[140:141], v[130:131], v[166:167]
	v_cvt_f32_i32_e32 v167, v93
	v_cvt_f32_i32_e32 v166, v92
	v_cvt_f32_i32_e32 v152, v110
	v_pk_mul_f32 v[158:159], v[132:133], v[158:159]
	v_cvt_f32_i32_e32 v161, v101
	v_cvt_f32_i32_e32 v160, v100
	v_pk_fma_f32 v[140:141], v[140:141], v[142:143], v[156:157] op_sel_hi:[1,0,0]
	v_pk_fma_f32 v[158:159], v[158:159], v[142:143], v[156:157] op_sel_hi:[1,0,0]
	v_cvt_f32_i32_e32 v171, v95
	v_cvt_f32_i32_e32 v170, v94
	v_pk_mul_f32 v[172:173], v[140:141], v[140:141]
	v_pk_mul_f32 v[140:141], v[124:125], v[166:167]
	v_pk_mul_f32 v[158:159], v[158:159], v[158:159]
	v_pk_fma_f32 v[166:167], v[140:141], v[142:143], v[156:157] op_sel_hi:[1,0,0]
	v_pk_mul_f32 v[152:153], v[138:139], v[152:153]
	v_cvt_pk_fp8_f32 v140, v164, v165
	v_cvt_pk_fp8_f32 v141, v158, v159
	v_pk_mul_f32 v[160:161], v[128:129], v[160:161]
	v_pk_fma_f32 v[152:153], v[152:153], v[142:143], v[156:157] op_sel_hi:[1,0,0]
	v_pk_fma_f32 v[160:161], v[160:161], v[142:143], v[156:157] op_sel_hi:[1,0,0]
	v_pk_mul_f32 v[170:171], v[126:127], v[170:171]
	v_pk_mul_f32 v[152:153], v[152:153], v[152:153]
	v_pk_mul_f32 v[160:161], v[160:161], v[160:161]
	v_pk_fma_f32 v[156:157], v[170:171], v[142:143], v[156:157] op_sel_hi:[1,0,0]
	v_pk_mul_f32 v[158:159], v[166:167], v[166:167]
	v_cvt_pk_fp8_f32 v140, v152, v153 op_sel:[0,0,1]
	v_cvt_pk_fp8_f32 v141, v168, v169 op_sel:[0,0,1]
	v_cvt_pk_fp8_f32 v142, v160, v161
	v_cvt_pk_fp8_f32 v143, v158, v159
	v_pk_mul_f32 v[152:153], v[156:157], v[156:157]
	v_or_b32_e32 v156, 16, v146
	v_cvt_pk_fp8_f32 v142, v172, v173 op_sel:[0,0,1]
	v_cvt_pk_fp8_f32 v143, v152, v153 op_sel:[0,0,1]
	v_ashrrev_i32_e32 v157, 31, v156
	v_mov_b64_e32 v[160:161], s[22:23]
	v_lshlrev_b64 v[152:153], 13, v[156:157]
	v_lshl_add_u64 v[152:153], s[10:11], 0, v[152:153]
	v_mfma_f32_16x16x32_fp8_fp8 v[156:159], v[140:141], v[160:161], 0
	v_lshl_add_u64 v[152:153], v[152:153], 0, v[144:145]
	global_store_dwordx4 v[152:153], v[140:143], off sc0 sc1
	s_nop 1
	v_mfma_f32_16x16x32_fp8_fp8 v[140:143], v[142:143], v[160:161], v[156:159]
	s_and_saveexec_b64 s[0:1], s[20:21]
	s_cbranch_execz .LBB2_72
	s_lshl_b32 s4, s64, 2
	s_or_b32 s4, s4, s46
	s_ashr_i32 s5, s4, 31
	s_lshl_b64 s[4:5], s[4:5], 14
	s_add_u32 s4, s2, s4
	s_addc_u32 s5, s3, s5
	v_lshl_add_u64 v[152:153], v[146:147], 2, s[4:5]
	v_lshlrev_b32_e32 v194, 2, v192
	v_lshl_add_u64 v[152:153], v[152:153], 0, v[194:195]
	global_store_dwordx4 v[152:153], v[140:143], off offset:64 sc0 sc1
.LBB2_72:
	s_or_b64 exec, exec, s[0:1]
	v_add_u32_e32 v155, 0x80, v162
	s_nop 3
	ds_read2st64_b32 v[142:143], v155 offset1:4
	v_cvt_f32_i32_e32 v141, v97
	v_cvt_f32_i32_e32 v140, v96
	v_cvt_f32_i32_e32 v161, v91
	v_cvt_f32_i32_e32 v160, v90
	s_waitcnt lgkmcnt(0)
	v_mov_b32_e32 v156, v143
	v_pk_mul_f32 v[140:141], v[136:137], v[140:141]
	v_cvt_f32_i32_e32 v167, v87
	v_cvt_f32_i32_e32 v166, v86
	v_pk_fma_f32 v[140:141], v[140:141], v[142:143], v[156:157] op_sel_hi:[1,0,0]
	v_cvt_f32_i32_e32 v159, v89
	v_pk_mul_f32 v[164:165], v[140:141], v[140:141]
	v_pk_mul_f32 v[140:141], v[134:135], v[160:161]
	v_cvt_f32_i32_e32 v158, v88
	v_pk_fma_f32 v[140:141], v[140:141], v[142:143], v[156:157] op_sel_hi:[1,0,0]
	v_cvt_f32_i32_e32 v153, v99
	v_pk_mul_f32 v[168:169], v[140:141], v[140:141]
	v_pk_mul_f32 v[140:141], v[130:131], v[166:167]
	v_cvt_f32_i32_e32 v167, v77
	v_cvt_f32_i32_e32 v166, v76
	v_cvt_f32_i32_e32 v152, v98
	v_pk_mul_f32 v[158:159], v[132:133], v[158:159]
	v_cvt_f32_i32_e32 v161, v85
	v_cvt_f32_i32_e32 v160, v84
	v_pk_fma_f32 v[140:141], v[140:141], v[142:143], v[156:157] op_sel_hi:[1,0,0]
	v_cvt_f32_i32_e32 v171, v79
	v_cvt_f32_i32_e32 v170, v78
	v_pk_fma_f32 v[158:159], v[158:159], v[142:143], v[156:157] op_sel_hi:[1,0,0]
	v_pk_mul_f32 v[172:173], v[140:141], v[140:141]
	v_pk_mul_f32 v[140:141], v[124:125], v[166:167]
	v_pk_mul_f32 v[158:159], v[158:159], v[158:159]
	v_pk_fma_f32 v[166:167], v[140:141], v[142:143], v[156:157] op_sel_hi:[1,0,0]
	v_pk_mul_f32 v[152:153], v[138:139], v[152:153]
	v_cvt_pk_fp8_f32 v140, v164, v165
	v_cvt_pk_fp8_f32 v141, v158, v159
	v_pk_mul_f32 v[160:161], v[128:129], v[160:161]
	v_pk_mul_f32 v[170:171], v[126:127], v[170:171]
	v_pk_fma_f32 v[152:153], v[152:153], v[142:143], v[156:157] op_sel_hi:[1,0,0]
	v_pk_fma_f32 v[160:161], v[160:161], v[142:143], v[156:157] op_sel_hi:[1,0,0]
	v_pk_fma_f32 v[142:143], v[170:171], v[142:143], v[156:157] op_sel_hi:[1,0,0]
	v_pk_mul_f32 v[152:153], v[152:153], v[152:153]
	v_pk_mul_f32 v[160:161], v[160:161], v[160:161]
	v_pk_mul_f32 v[156:157], v[166:167], v[166:167]
	v_pk_mul_f32 v[164:165], v[142:143], v[142:143]
	v_cvt_pk_fp8_f32 v140, v152, v153 op_sel:[0,0,1]
	v_cvt_pk_fp8_f32 v142, v160, v161
	v_cvt_pk_fp8_f32 v143, v156, v157
	v_cvt_pk_fp8_f32 v141, v168, v169 op_sel:[0,0,1]
	s_mov_b32 s23, s22
	v_cvt_pk_fp8_f32 v142, v172, v173 op_sel:[0,0,1]
	v_cvt_pk_fp8_f32 v143, v164, v165 op_sel:[0,0,1]
	v_or_b32_e32 v152, 32, v146
	v_mov_b64_e32 v[160:161], s[22:23]
	v_ashrrev_i32_e32 v153, 31, v152
	v_lshlrev_b64 v[152:153], 13, v[152:153]
	v_mfma_f32_16x16x32_fp8_fp8 v[156:159], v[140:141], v[160:161], 0
	v_lshl_add_u64 v[152:153], s[10:11], 0, v[152:153]
	v_lshl_add_u64 v[152:153], v[152:153], 0, v[144:145]
	global_store_dwordx4 v[152:153], v[140:143], off sc0 sc1
	s_nop 1
	v_mfma_f32_16x16x32_fp8_fp8 v[140:143], v[142:143], v[160:161], v[156:159]
	s_and_saveexec_b64 s[0:1], s[20:21]
	s_cbranch_execz .LBB2_74
	s_lshl_b32 s4, s64, 2
	s_or_b32 s4, s4, s46
	s_ashr_i32 s5, s4, 31
	s_lshl_b64 s[4:5], s[4:5], 14
	s_add_u32 s4, s2, s4
	s_addc_u32 s5, s3, s5
	v_lshl_add_u64 v[152:153], v[146:147], 2, s[4:5]
	v_lshlrev_b32_e32 v194, 2, v192
	v_lshl_add_u64 v[152:153], v[152:153], 0, v[194:195]
	global_store_dwordx4 v[152:153], v[140:143], off offset:128 sc0 sc1
.LBB2_74:
	s_or_b64 exec, exec, s[0:1]
	v_add_u32_e32 v156, 0xc0, v162
	s_nop 3
	ds_read2st64_b32 v[142:143], v156 offset1:4
	v_cvt_f32_i32_e32 v141, v81
	v_cvt_f32_i32_e32 v140, v80
	v_cvt_f32_i32_e32 v165, v75
	v_cvt_f32_i32_e32 v164, v74
	s_waitcnt lgkmcnt(0)
	v_mov_b32_e32 v158, v143
	v_pk_mul_f32 v[140:141], v[136:137], v[140:141]
	v_cvt_f32_i32_e32 v169, v71
	v_cvt_f32_i32_e32 v168, v70
	v_pk_fma_f32 v[140:141], v[140:141], v[142:143], v[158:159] op_sel_hi:[1,0,0]
	v_cvt_f32_i32_e32 v161, v73
	v_pk_mul_f32 v[166:167], v[140:141], v[140:141]
	v_pk_mul_f32 v[140:141], v[134:135], v[164:165]
	v_cvt_f32_i32_e32 v160, v72
	v_pk_fma_f32 v[140:141], v[140:141], v[142:143], v[158:159] op_sel_hi:[1,0,0]
	v_cvt_f32_i32_e32 v153, v83
	v_pk_mul_f32 v[170:171], v[140:141], v[140:141]
	v_pk_mul_f32 v[140:141], v[130:131], v[168:169]
	v_cvt_f32_i32_e32 v169, v65
	v_cvt_f32_i32_e32 v168, v64
	v_cvt_f32_i32_e32 v152, v82
	v_pk_mul_f32 v[160:161], v[132:133], v[160:161]
	v_cvt_f32_i32_e32 v165, v69
	v_cvt_f32_i32_e32 v164, v68
	v_pk_fma_f32 v[140:141], v[140:141], v[142:143], v[158:159] op_sel_hi:[1,0,0]
	v_pk_fma_f32 v[160:161], v[160:161], v[142:143], v[158:159] op_sel_hi:[1,0,0]
	v_cvt_f32_i32_e32 v173, v67
	v_cvt_f32_i32_e32 v172, v66
	v_pk_mul_f32 v[174:175], v[140:141], v[140:141]
	v_pk_mul_f32 v[140:141], v[124:125], v[168:169]
	v_pk_mul_f32 v[160:161], v[160:161], v[160:161]
	v_pk_fma_f32 v[168:169], v[140:141], v[142:143], v[158:159] op_sel_hi:[1,0,0]
	v_pk_mul_f32 v[152:153], v[138:139], v[152:153]
	v_cvt_pk_fp8_f32 v140, v166, v167
	v_cvt_pk_fp8_f32 v141, v160, v161
	v_pk_mul_f32 v[164:165], v[128:129], v[164:165]
	v_pk_fma_f32 v[152:153], v[152:153], v[142:143], v[158:159] op_sel_hi:[1,0,0]
	v_pk_fma_f32 v[164:165], v[164:165], v[142:143], v[158:159] op_sel_hi:[1,0,0]
	v_pk_mul_f32 v[172:173], v[126:127], v[172:173]
	v_pk_mul_f32 v[152:153], v[152:153], v[152:153]
	v_pk_mul_f32 v[164:165], v[164:165], v[164:165]
	v_pk_fma_f32 v[158:159], v[172:173], v[142:143], v[158:159] op_sel_hi:[1,0,0]
	v_pk_mul_f32 v[160:161], v[168:169], v[168:169]
	v_cvt_pk_fp8_f32 v140, v152, v153 op_sel:[0,0,1]
	v_cvt_pk_fp8_f32 v141, v170, v171 op_sel:[0,0,1]
	v_cvt_pk_fp8_f32 v142, v164, v165
	v_cvt_pk_fp8_f32 v143, v160, v161
	v_pk_mul_f32 v[152:153], v[158:159], v[158:159]
	v_or_b32_e32 v158, 48, v146
	v_cvt_pk_fp8_f32 v142, v174, v175 op_sel:[0,0,1]
	v_cvt_pk_fp8_f32 v143, v152, v153 op_sel:[0,0,1]
	v_ashrrev_i32_e32 v159, 31, v158
	v_mov_b64_e32 v[164:165], s[22:23]
	v_lshlrev_b64 v[152:153], 13, v[158:159]
	v_lshl_add_u64 v[152:153], s[10:11], 0, v[152:153]
	v_mfma_f32_16x16x32_fp8_fp8 v[158:161], v[140:141], v[164:165], 0
	v_lshl_add_u64 v[152:153], v[152:153], 0, v[144:145]
	global_store_dwordx4 v[152:153], v[140:143], off sc0 sc1
	s_nop 1
	v_mfma_f32_16x16x32_fp8_fp8 v[140:143], v[142:143], v[164:165], v[158:161]
	s_and_saveexec_b64 s[0:1], s[20:21]
	s_cbranch_execz .LBB2_76
	s_lshl_b32 s4, s64, 2
	s_or_b32 s4, s4, s46
	s_ashr_i32 s5, s4, 31
	s_lshl_b64 s[4:5], s[4:5], 14
	s_add_u32 s4, s2, s4
	s_addc_u32 s5, s3, s5
	v_lshl_add_u64 v[152:153], v[146:147], 2, s[4:5]
	v_lshlrev_b32_e32 v194, 2, v192
	v_lshl_add_u64 v[152:153], v[152:153], 0, v[194:195]
	global_store_dwordx4 v[152:153], v[140:143], off offset:192 sc0 sc1
.LBB2_76:
	s_or_b64 exec, exec, s[0:1]
	s_nop 4
	ds_read2st64_b32 v[140:141], v162 offset0:2 offset1:6
	v_cvt_f32_i32_e32 v143, v61
	v_cvt_f32_i32_e32 v153, v63
	v_cvt_f32_i32_e32 v152, v62
	v_cvt_f32_i32_e32 v142, v60
	v_cvt_f32_i32_e32 v161, v57
	v_cvt_f32_i32_e32 v165, v59
	v_cvt_f32_i32_e32 v164, v58
	v_cvt_f32_i32_e32 v160, v56
	v_cvt_f32_i32_e32 v167, v49
	v_cvt_f32_i32_e32 v169, v51
	v_cvt_f32_i32_e32 v168, v50
	v_cvt_f32_i32_e32 v166, v48
	v_cvt_f32_i32_e32 v171, v41
	v_cvt_f32_i32_e32 v173, v43
	v_cvt_f32_i32_e32 v172, v42
	v_cvt_f32_i32_e32 v170, v40
	v_pk_mul_f32 v[152:153], v[138:139], v[152:153]
	v_pk_mul_f32 v[142:143], v[136:137], v[142:143]
	s_waitcnt lgkmcnt(0)
	v_mov_b32_e32 v158, v141
	v_pk_mul_f32 v[164:165], v[134:135], v[164:165]
	v_pk_mul_f32 v[160:161], v[132:133], v[160:161]
	v_pk_mul_f32 v[168:169], v[130:131], v[168:169]
	v_pk_mul_f32 v[166:167], v[128:129], v[166:167]
	v_pk_mul_f32 v[172:173], v[126:127], v[172:173]
	v_pk_mul_f32 v[170:171], v[124:125], v[170:171]
	v_pk_fma_f32 v[142:143], v[142:143], v[140:141], v[158:159] op_sel_hi:[1,0,0]
	v_pk_fma_f32 v[152:153], v[152:153], v[140:141], v[158:159] op_sel_hi:[1,0,0]
	v_pk_fma_f32 v[160:161], v[160:161], v[140:141], v[158:159] op_sel_hi:[1,0,0]
	v_pk_fma_f32 v[164:165], v[164:165], v[140:141], v[158:159] op_sel_hi:[1,0,0]
	v_pk_fma_f32 v[166:167], v[166:167], v[140:141], v[158:159] op_sel_hi:[1,0,0]
	v_pk_fma_f32 v[168:169], v[168:169], v[140:141], v[158:159] op_sel_hi:[1,0,0]
	v_pk_fma_f32 v[170:171], v[170:171], v[140:141], v[158:159] op_sel_hi:[1,0,0]
	v_pk_fma_f32 v[140:141], v[172:173], v[140:141], v[158:159] op_sel_hi:[1,0,0]
	v_pk_mul_f32 v[142:143], v[142:143], v[142:143]
	v_pk_mul_f32 v[160:161], v[160:161], v[160:161]
	v_pk_mul_f32 v[158:159], v[170:171], v[170:171]
	v_pk_mul_f32 v[170:171], v[140:141], v[140:141]
	v_pk_mul_f32 v[152:153], v[152:153], v[152:153]
	v_cvt_pk_fp8_f32 v140, v142, v143
	v_cvt_pk_fp8_f32 v141, v160, v161
	v_pk_mul_f32 v[164:165], v[164:165], v[164:165]
	v_pk_mul_f32 v[166:167], v[166:167], v[166:167]
	v_cvt_pk_fp8_f32 v140, v152, v153 op_sel:[0,0,1]
	v_cvt_pk_fp8_f32 v142, v166, v167
	v_cvt_pk_fp8_f32 v143, v158, v159
	v_cvt_pk_fp8_f32 v141, v164, v165 op_sel:[0,0,1]
	v_pk_mul_f32 v[168:169], v[168:169], v[168:169]
	s_mov_b32 s23, s22
	v_cvt_pk_fp8_f32 v142, v168, v169 op_sel:[0,0,1]
	v_cvt_pk_fp8_f32 v143, v170, v171 op_sel:[0,0,1]
	v_lshlrev_b64 v[152:153], 13, v[146:147]
	v_mov_b64_e32 v[166:167], s[22:23]
	v_lshl_add_u64 v[152:153], s[10:11], 0, v[152:153]
	v_lshl_add_u64 v[152:153], v[152:153], 0, v[144:145]
	v_mfma_f32_16x16x32_fp8_fp8 v[158:161], v[140:141], v[166:167], 0
	v_add_co_u32_e32 v164, vcc, s56, v152
	s_nop 1
	v_addc_co_u32_e32 v165, vcc, 0, v153, vcc
	global_store_dwordx4 v[164:165], v[140:143], off sc0 sc1
	s_nop 1
	v_mfma_f32_16x16x32_fp8_fp8 v[140:143], v[142:143], v[166:167], v[158:161]
	s_and_saveexec_b64 s[0:1], s[20:21]
	s_cbranch_execz .LBB2_78
	s_lshl_b32 s4, s64, 2
	s_or_b32 s4, s4, s46
	s_ashr_i32 s5, s4, 31
	s_lshl_b64 s[4:5], s[4:5], 14
	s_add_u32 s4, s2, s4
	s_addc_u32 s5, s3, s5
	v_lshl_add_u64 v[158:159], v[146:147], 2, s[4:5]
	v_lshlrev_b32_e32 v194, 2, v192
	v_lshl_add_u64 v[158:159], v[158:159], 0, v[194:195]
	global_store_dwordx4 v[158:159], v[140:143], off offset:512 sc0 sc1
.LBB2_78:
	s_or_b64 exec, exec, s[0:1]
	ds_read2st64_b32 v[158:159], v154 offset0:2 offset1:6
	s_nop 3
	v_cvt_f32_i32_e32 v141, v53
	v_cvt_f32_i32_e32 v140, v52
	v_cvt_f32_i32_e32 v165, v47
	v_cvt_f32_i32_e32 v164, v46
	s_waitcnt lgkmcnt(0)
	v_mov_b32_e32 v154, v159
	v_pk_mul_f32 v[140:141], v[136:137], v[140:141]
	v_cvt_f32_i32_e32 v169, v35
	v_cvt_f32_i32_e32 v168, v34
	v_pk_fma_f32 v[140:141], v[140:141], v[158:159], v[154:155] op_sel_hi:[1,0,0]
	v_cvt_f32_i32_e32 v161, v45
	v_cvt_f32_i32_e32 v160, v44
	v_pk_mul_f32 v[166:167], v[140:141], v[140:141]
	v_pk_mul_f32 v[140:141], v[134:135], v[164:165]
	v_cvt_f32_i32_e32 v143, v55
	v_pk_fma_f32 v[140:141], v[140:141], v[158:159], v[154:155] op_sel_hi:[1,0,0]
	v_cvt_f32_i32_e32 v142, v54
	v_pk_mul_f32 v[170:171], v[140:141], v[140:141]
	v_pk_mul_f32 v[140:141], v[130:131], v[168:169]
	v_pk_mul_f32 v[160:161], v[132:133], v[160:161]
	v_cvt_f32_i32_e32 v165, v33
	v_cvt_f32_i32_e32 v164, v32
	v_pk_fma_f32 v[140:141], v[140:141], v[158:159], v[154:155] op_sel_hi:[1,0,0]
	v_cvt_f32_i32_e32 v169, v25
	v_cvt_f32_i32_e32 v168, v24
	v_pk_fma_f32 v[160:161], v[160:161], v[158:159], v[154:155] op_sel_hi:[1,0,0]
	v_pk_mul_f32 v[174:175], v[140:141], v[140:141]
	v_pk_mul_f32 v[160:161], v[160:161], v[160:161]
	v_cvt_pk_fp8_f32 v140, v166, v167
	v_pk_mul_f32 v[142:143], v[138:139], v[142:143]
	v_cvt_pk_fp8_f32 v141, v160, v161
	v_pk_fma_f32 v[142:143], v[142:143], v[158:159], v[154:155] op_sel_hi:[1,0,0]
	v_pk_mul_f32 v[164:165], v[128:129], v[164:165]
	v_cvt_f32_i32_e32 v173, v27
	v_cvt_f32_i32_e32 v172, v26
	v_pk_mul_f32 v[168:169], v[124:125], v[168:169]
	v_pk_mul_f32 v[142:143], v[142:143], v[142:143]
	v_pk_fma_f32 v[164:165], v[164:165], v[158:159], v[154:155] op_sel_hi:[1,0,0]
	v_pk_fma_f32 v[160:161], v[168:169], v[158:159], v[154:155] op_sel_hi:[1,0,0]
	v_pk_mul_f32 v[164:165], v[164:165], v[164:165]
	v_pk_mul_f32 v[160:161], v[160:161], v[160:161]
	v_cvt_pk_fp8_f32 v140, v142, v143 op_sel:[0,0,1]
	v_cvt_pk_fp8_f32 v141, v170, v171 op_sel:[0,0,1]
	v_cvt_pk_fp8_f32 v142, v164, v165
	v_cvt_pk_fp8_f32 v143, v160, v161
	v_pk_mul_f32 v[172:173], v[126:127], v[172:173]
	v_mov_b64_e32 v[164:165], s[22:23]
	v_pk_fma_f32 v[158:159], v[172:173], v[158:159], v[154:155] op_sel_hi:[1,0,0]
	v_cvt_pk_fp8_f32 v142, v174, v175 op_sel:[0,0,1]
	v_pk_mul_f32 v[158:159], v[158:159], v[158:159]
	v_add_co_u32_e32 v152, vcc, 0x120000, v152
	v_cvt_pk_fp8_f32 v143, v158, v159 op_sel:[0,0,1]
	v_mfma_f32_16x16x32_fp8_fp8 v[158:161], v[140:141], v[164:165], 0
	v_addc_co_u32_e32 v153, vcc, 0, v153, vcc
	global_store_dwordx4 v[152:153], v[140:143], off sc0 sc1
	s_nop 1
	v_mfma_f32_16x16x32_fp8_fp8 v[140:143], v[142:143], v[164:165], v[158:161]
	s_and_saveexec_b64 s[0:1], s[20:21]
	s_cbranch_execz .LBB2_80
	s_lshl_b32 s4, s64, 2
	s_or_b32 s4, s4, s46
	s_ashr_i32 s5, s4, 31
	s_lshl_b64 s[4:5], s[4:5], 14
	s_add_u32 s4, s2, s4
	s_addc_u32 s5, s3, s5
	v_lshl_add_u64 v[152:153], v[146:147], 2, s[4:5]
	v_lshlrev_b32_e32 v194, 2, v192
	v_lshl_add_u64 v[152:153], v[152:153], 0, v[194:195]
	global_store_dwordx4 v[152:153], v[140:143], off offset:576 sc0 sc1
.LBB2_80:
	s_or_b64 exec, exec, s[0:1]
	s_nop 4
	ds_read2st64_b32 v[140:141], v155 offset0:2 offset1:6
	v_cvt_f32_i32_e32 v143, v37
	v_cvt_f32_i32_e32 v153, v39
	v_cvt_f32_i32_e32 v152, v38
	v_cvt_f32_i32_e32 v142, v36
	v_cvt_f32_i32_e32 v159, v29
	v_cvt_f32_i32_e32 v161, v31
	v_cvt_f32_i32_e32 v160, v30
	v_cvt_f32_i32_e32 v158, v28
	v_cvt_f32_i32_e32 v165, v17
	v_cvt_f32_i32_e32 v167, v19
	v_cvt_f32_i32_e32 v166, v18
	v_cvt_f32_i32_e32 v164, v16
	v_cvt_f32_i32_e32 v169, v9
	v_cvt_f32_i32_e32 v171, v11
	v_cvt_f32_i32_e32 v170, v10
	v_cvt_f32_i32_e32 v168, v8
	v_pk_mul_f32 v[152:153], v[138:139], v[152:153]
	v_pk_mul_f32 v[142:143], v[136:137], v[142:143]
	s_waitcnt lgkmcnt(0)
	v_mov_b32_e32 v154, v141
	v_pk_mul_f32 v[160:161], v[134:135], v[160:161]
	v_pk_mul_f32 v[158:159], v[132:133], v[158:159]
	v_pk_mul_f32 v[166:167], v[130:131], v[166:167]
	v_pk_mul_f32 v[164:165], v[128:129], v[164:165]
	v_pk_mul_f32 v[170:171], v[126:127], v[170:171]
	v_pk_mul_f32 v[168:169], v[124:125], v[168:169]
	v_pk_fma_f32 v[142:143], v[142:143], v[140:141], v[154:155] op_sel_hi:[1,0,0]
	v_pk_fma_f32 v[152:153], v[152:153], v[140:141], v[154:155] op_sel_hi:[1,0,0]
	v_pk_fma_f32 v[158:159], v[158:159], v[140:141], v[154:155] op_sel_hi:[1,0,0]
	v_pk_fma_f32 v[160:161], v[160:161], v[140:141], v[154:155] op_sel_hi:[1,0,0]
	v_pk_fma_f32 v[164:165], v[164:165], v[140:141], v[154:155] op_sel_hi:[1,0,0]
	v_pk_fma_f32 v[166:167], v[166:167], v[140:141], v[154:155] op_sel_hi:[1,0,0]
	v_pk_fma_f32 v[168:169], v[168:169], v[140:141], v[154:155] op_sel_hi:[1,0,0]
	v_pk_fma_f32 v[140:141], v[170:171], v[140:141], v[154:155] op_sel_hi:[1,0,0]
	v_pk_mul_f32 v[142:143], v[142:143], v[142:143]
	v_pk_mul_f32 v[158:159], v[158:159], v[158:159]
	v_pk_mul_f32 v[154:155], v[168:169], v[168:169]
	v_pk_mul_f32 v[168:169], v[140:141], v[140:141]
	v_pk_mul_f32 v[152:153], v[152:153], v[152:153]
	v_cvt_pk_fp8_f32 v140, v142, v143
	v_cvt_pk_fp8_f32 v141, v158, v159
	v_pk_mul_f32 v[160:161], v[160:161], v[160:161]
	v_pk_mul_f32 v[164:165], v[164:165], v[164:165]
	v_cvt_pk_fp8_f32 v140, v152, v153 op_sel:[0,0,1]
	v_cvt_pk_fp8_f32 v142, v164, v165
	v_cvt_pk_fp8_f32 v143, v154, v155
	v_cvt_pk_fp8_f32 v141, v160, v161 op_sel:[0,0,1]
	v_pk_mul_f32 v[166:167], v[166:167], v[166:167]
	v_lshlrev_b64 v[152:153], 13, v[146:147]
	v_cvt_pk_fp8_f32 v142, v166, v167 op_sel:[0,0,1]
	v_cvt_pk_fp8_f32 v143, v168, v169 op_sel:[0,0,1]
	s_mov_b32 s23, s22
	v_lshl_add_u64 v[152:153], s[10:11], 0, v[152:153]
	v_mov_b64_e32 v[160:161], s[22:23]
	v_lshl_add_u64 v[158:159], v[152:153], 0, v[144:145]
	v_add_co_u32_e32 v158, vcc, s57, v158
	v_mfma_f32_16x16x32_fp8_fp8 v[152:155], v[140:141], v[160:161], 0
	s_nop 0
	v_addc_co_u32_e32 v159, vcc, 0, v159, vcc
	global_store_dwordx4 v[158:159], v[140:143], off sc0 sc1
	s_nop 1
	v_mfma_f32_16x16x32_fp8_fp8 v[140:143], v[142:143], v[160:161], v[152:155]
	s_and_saveexec_b64 s[0:1], s[20:21]
	s_cbranch_execz .LBB2_82
	s_lshl_b32 s4, s64, 2
	s_or_b32 s4, s4, s46
	s_ashr_i32 s5, s4, 31
	s_lshl_b64 s[4:5], s[4:5], 14
	s_add_u32 s4, s2, s4
	s_addc_u32 s5, s3, s5
	v_lshl_add_u64 v[152:153], v[146:147], 2, s[4:5]
	v_lshlrev_b32_e32 v194, 2, v192
	v_lshl_add_u64 v[152:153], v[152:153], 0, v[194:195]
	global_store_dwordx4 v[152:153], v[140:143], off offset:640 sc0 sc1
.LBB2_82:
	s_or_b64 exec, exec, s[0:1]
	v_cvt_f32_i32_e32 v153, v23
	v_cvt_f32_i32_e32 v152, v22
	v_cvt_f32_i32_e32 v155, v15
	v_cvt_f32_i32_e32 v154, v14
	s_nop 0
	ds_read2st64_b32 v[140:141], v156 offset0:2 offset1:6
	v_pk_mul_f32 v[138:139], v[138:139], v[152:153]
	v_cvt_f32_i32_e32 v153, v13
	v_cvt_f32_i32_e32 v152, v12
	v_cvt_f32_i32_e32 v143, v21
	v_cvt_f32_i32_e32 v142, v20
	v_pk_mul_f32 v[134:135], v[134:135], v[154:155]
	v_pk_mul_f32 v[132:133], v[132:133], v[152:153]
	v_cvt_f32_i32_e32 v153, v5
	v_cvt_f32_i32_e32 v152, v4
	v_cvt_f32_i32_e32 v155, v7
	v_cvt_f32_i32_e32 v154, v6
	v_pk_mul_f32 v[136:137], v[136:137], v[142:143]
	v_pk_mul_f32 v[128:129], v[128:129], v[152:153]
	v_cvt_f32_i32_e32 v153, v1
	v_cvt_f32_i32_e32 v152, v0
	s_waitcnt lgkmcnt(0)
	v_mov_b32_e32 v142, v141
	v_pk_fma_f32 v[136:137], v[136:137], v[140:141], v[142:143] op_sel_hi:[1,0,0]
	v_pk_fma_f32 v[132:133], v[132:133], v[140:141], v[142:143] op_sel_hi:[1,0,0]
	v_pk_mul_f32 v[130:131], v[130:131], v[154:155]
	v_cvt_f32_i32_e32 v155, v3
	v_cvt_f32_i32_e32 v154, v2
	v_pk_mul_f32 v[124:125], v[124:125], v[152:153]
	v_pk_mul_f32 v[136:137], v[136:137], v[136:137]
	v_pk_mul_f32 v[132:133], v[132:133], v[132:133]
	v_pk_fma_f32 v[152:153], v[124:125], v[140:141], v[142:143] op_sel_hi:[1,0,0]
	v_pk_fma_f32 v[138:139], v[138:139], v[140:141], v[142:143] op_sel_hi:[1,0,0]
	v_cvt_pk_fp8_f32 v124, v136, v137
	v_cvt_pk_fp8_f32 v125, v132, v133
	v_pk_fma_f32 v[134:135], v[134:135], v[140:141], v[142:143] op_sel_hi:[1,0,0]
	v_pk_fma_f32 v[128:129], v[128:129], v[140:141], v[142:143] op_sel_hi:[1,0,0]
	v_pk_mul_f32 v[126:127], v[126:127], v[154:155]
	v_pk_mul_f32 v[138:139], v[138:139], v[138:139]
	v_pk_mul_f32 v[134:135], v[134:135], v[134:135]
	v_pk_mul_f32 v[128:129], v[128:129], v[128:129]
	v_pk_fma_f32 v[132:133], v[126:127], v[140:141], v[142:143] op_sel_hi:[1,0,0]
	v_pk_mul_f32 v[136:137], v[152:153], v[152:153]
	v_cvt_pk_fp8_f32 v124, v138, v139 op_sel:[0,0,1]
	v_cvt_pk_fp8_f32 v125, v134, v135 op_sel:[0,0,1]
	v_cvt_pk_fp8_f32 v126, v128, v129
	v_cvt_pk_fp8_f32 v127, v136, v137
	v_pk_fma_f32 v[130:131], v[130:131], v[140:141], v[142:143] op_sel_hi:[1,0,0]
	v_pk_mul_f32 v[128:129], v[132:133], v[132:133]
	v_pk_mul_f32 v[130:131], v[130:131], v[130:131]
	v_cvt_pk_fp8_f32 v127, v128, v129 op_sel:[0,0,1]
	v_cvt_pk_fp8_f32 v126, v130, v131 op_sel:[0,0,1]
	v_mov_b64_e32 v[134:135], s[22:23]
	v_add_u32_e32 v160, 0xb0, v146
	v_ashrrev_i32_e32 v161, 31, v160
	v_mfma_f32_16x16x32_fp8_fp8 v[128:131], v[124:125], v[134:135], 0
	v_lshlrev_b64 v[132:133], 13, v[160:161]
	v_lshl_add_u64 v[132:133], s[10:11], 0, v[132:133]
	v_lshl_add_u64 v[132:133], v[132:133], 0, v[144:145]
	v_mfma_f32_16x16x32_fp8_fp8 v[140:143], v[126:127], v[134:135], v[128:131]
	s_mov_b64 s[0:1], s[20:21]
	global_store_dwordx4 v[132:133], v[124:127], off sc0 sc1
.LBB2_83:
	s_and_saveexec_b64 s[4:5], s[0:1]
	s_cbranch_execz .LBB2_85
	s_lshl_b32 s0, s64, 2
	s_or_b32 s0, s0, s46
	s_ashr_i32 s1, s0, 31
	s_lshl_b64 s[0:1], s[0:1], 14
	s_add_u32 s0, s2, s0
	s_addc_u32 s1, s3, s1
	s_waitcnt lgkmcnt(0)
	v_lshl_add_u64 v[124:125], v[160:161], 2, s[0:1]
	v_lshlrev_b32_e32 v194, 2, v192
	v_lshl_add_u64 v[124:125], v[124:125], 0, v[194:195]
	global_store_dwordx4 v[124:125], v[140:143], off sc0 sc1

.LBB2_86:
	s_andn2_b64 vcc, exec, s[0:1]
	s_cbranch_vccnz .LBB2_25
	s_waitcnt lgkmcnt(2)
	ds_read_b128 v[132:135], v163
	ds_read_b32 v152, v162 offset:2048
	ds_read_b128 v[136:139], v163 offset:1024
	s_waitcnt lgkmcnt(4)
	ds_read_b128 v[128:131], v163 offset:16
	s_waitcnt lgkmcnt(4)
	ds_read_b128 v[124:127], v163 offset:1040
	v_cvt_f32_i32_e32 v121, v121
	v_cvt_f32_i32_e32 v123, v123
	v_cvt_f32_i32_e32 v122, v122
	v_cvt_f32_i32_e32 v120, v120
	s_waitcnt lgkmcnt(3)
	v_pk_mul_f32 v[140:141], v[132:133], v[152:153] op_sel_hi:[1,0]
	v_pk_mul_f32 v[142:143], v[134:135], v[152:153] op_sel_hi:[1,0]
	s_waitcnt lgkmcnt(2)
	v_pk_fma_f32 v[148:149], v[140:141], v[148:149], v[136:137]
	v_pk_fma_f32 v[154:155], v[142:143], v[150:151], v[138:139]
	s_waitcnt lgkmcnt(1)
	v_pk_mul_f32 v[140:141], v[128:129], v[152:153] op_sel_hi:[1,0]
	v_pk_mul_f32 v[142:143], v[130:131], v[152:153] op_sel_hi:[1,0]
	s_waitcnt lgkmcnt(0)
	v_pk_fma_f32 v[158:159], v[140:141], v[120:121], v[124:125]
	v_pk_fma_f32 v[156:157], v[142:143], v[122:123], v[126:127]
	ds_read_b128 v[140:143], v163 offset:32
	ds_read_b128 v[120:123], v163 offset:1056
	v_cvt_f32_i32_e32 v161, v119
	v_cvt_f32_i32_e32 v160, v118
	v_cvt_f32_i32_e32 v165, v113
	v_cvt_f32_i32_e32 v164, v112
	v_cvt_f32_i32_e32 v167, v115
	v_cvt_f32_i32_e32 v166, v114
	ds_read_b128 v[112:115], v163 offset:48
	v_cvt_f32_i32_e32 v151, v117
	v_cvt_f32_i32_e32 v150, v116
	ds_read_b128 v[116:119], v163 offset:1072
	s_waitcnt lgkmcnt(3)
	v_pk_mul_f32 v[168:169], v[142:143], v[152:153] op_sel_hi:[1,0]
	v_pk_mul_f32 v[148:149], v[148:149], v[148:149]
	s_waitcnt lgkmcnt(2)
	v_pk_fma_f32 v[160:161], v[168:169], v[160:161], v[122:123]
	v_pk_mul_f32 v[168:169], v[140:141], v[152:153] op_sel_hi:[1,0]
	v_ashrrev_i32_e32 v147, 31, v146
	v_pk_fma_f32 v[168:169], v[168:169], v[150:151], v[120:121]
	s_waitcnt lgkmcnt(1)
	v_pk_mul_f32 v[150:151], v[114:115], v[152:153] op_sel_hi:[1,0]
	v_cvt_f32_i32_e32 v109, v109
	s_waitcnt lgkmcnt(0)
	v_pk_fma_f32 v[166:167], v[150:151], v[166:167], v[118:119]
	v_pk_mul_f32 v[150:151], v[112:113], v[152:153] op_sel_hi:[1,0]
	v_cvt_f32_i32_e32 v108, v108
	v_pk_fma_f32 v[164:165], v[150:151], v[164:165], v[116:117]
	v_cvt_f32_i32_e32 v111, v111
	v_cvt_pk_fp8_f32 v150, v148, v149
	v_pk_mul_f32 v[148:149], v[158:159], v[158:159]
	v_cvt_f32_i32_e32 v110, v110
	v_cvt_pk_fp8_f32 v151, v148, v149
	v_pk_mul_f32 v[148:149], v[168:169], v[168:169]
	v_cvt_f32_i32_e32 v105, v105
	v_cvt_pk_fp8_f32 v152, v148, v149
	v_pk_mul_f32 v[148:149], v[164:165], v[164:165]
	v_cvt_f32_i32_e32 v104, v104
	v_cvt_pk_fp8_f32 v153, v148, v149
	v_pk_mul_f32 v[148:149], v[154:155], v[154:155]
	v_pk_mul_f32 v[154:155], v[166:167], v[166:167]
	v_cvt_pk_fp8_f32 v150, v148, v149 op_sel:[0,0,1]
	v_pk_mul_f32 v[148:149], v[156:157], v[156:157]
	v_cvt_pk_fp8_f32 v153, v154, v155 op_sel:[0,0,1]
	v_cvt_pk_fp8_f32 v151, v148, v149 op_sel:[0,0,1]
	v_pk_mul_f32 v[148:149], v[160:161], v[160:161]
	v_cvt_f32_i32_e32 v107, v107
	v_cvt_pk_fp8_f32 v152, v148, v149 op_sel:[0,0,1]
	v_lshlrev_b64 v[148:149], 11, v[146:147]
	v_lshl_add_u64 v[148:149], s[8:9], 0, v[148:149]
	v_lshl_add_u64 v[148:149], v[148:149], 0, v[144:145]
	global_store_dwordx4 v[148:149], v[150:153], off sc0 sc1
	ds_read_b32 v150, v162 offset:2112
	v_cvt_f32_i32_e32 v106, v106
	v_cvt_f32_i32_e32 v101, v101
	v_cvt_f32_i32_e32 v100, v100
	v_cvt_f32_i32_e32 v93, v93
	s_waitcnt lgkmcnt(0)
	v_pk_mul_f32 v[152:153], v[132:133], v[150:151] op_sel_hi:[1,0]
	v_cvt_f32_i32_e32 v95, v95
	v_cvt_f32_i32_e32 v94, v94
	v_cvt_f32_i32_e32 v92, v92
	v_pk_mul_f32 v[154:155], v[134:135], v[150:151] op_sel_hi:[1,0]
	v_pk_fma_f32 v[108:109], v[152:153], v[108:109], v[136:137]
	v_pk_mul_f32 v[152:153], v[128:129], v[150:151] op_sel_hi:[1,0]
	v_pk_fma_f32 v[110:111], v[154:155], v[110:111], v[138:139]
	v_pk_mul_f32 v[154:155], v[130:131], v[150:151] op_sel_hi:[1,0]
	v_pk_fma_f32 v[104:105], v[152:153], v[104:105], v[124:125]
	v_pk_mul_f32 v[152:153], v[140:141], v[150:151] op_sel_hi:[1,0]
	v_pk_fma_f32 v[106:107], v[154:155], v[106:107], v[126:127]
	v_pk_mul_f32 v[154:155], v[142:143], v[150:151] op_sel_hi:[1,0]
	v_pk_fma_f32 v[100:101], v[152:153], v[100:101], v[120:121]
	v_pk_mul_f32 v[152:153], v[112:113], v[150:151] op_sel_hi:[1,0]
	v_pk_mul_f32 v[150:151], v[114:115], v[150:151] op_sel_hi:[1,0]
	v_cvt_f32_i32_e32 v103, v103
	v_cvt_f32_i32_e32 v102, v102
	v_pk_fma_f32 v[94:95], v[150:151], v[94:95], v[118:119]
	v_pk_fma_f32 v[92:93], v[152:153], v[92:93], v[116:117]
	v_pk_mul_f32 v[108:109], v[108:109], v[108:109]
	v_pk_mul_f32 v[104:105], v[104:105], v[104:105]
	v_pk_mul_f32 v[100:101], v[100:101], v[100:101]
	v_pk_mul_f32 v[150:151], v[94:95], v[94:95]
	v_pk_mul_f32 v[152:153], v[92:93], v[92:93]
	v_pk_fma_f32 v[102:103], v[154:155], v[102:103], v[122:123]
	v_cvt_pk_fp8_f32 v92, v108, v109
	v_cvt_pk_fp8_f32 v93, v104, v105
	v_cvt_pk_fp8_f32 v94, v100, v101
	v_cvt_pk_fp8_f32 v95, v152, v153
	v_pk_mul_f32 v[110:111], v[110:111], v[110:111]
	v_pk_mul_f32 v[106:107], v[106:107], v[106:107]
	v_pk_mul_f32 v[102:103], v[102:103], v[102:103]
	v_or_b32_e32 v100, 16, v146
	v_cvt_pk_fp8_f32 v92, v110, v111 op_sel:[0,0,1]
	v_cvt_pk_fp8_f32 v93, v106, v107 op_sel:[0,0,1]
	v_cvt_pk_fp8_f32 v94, v102, v103 op_sel:[0,0,1]
	v_cvt_pk_fp8_f32 v95, v150, v151 op_sel:[0,0,1]
	v_ashrrev_i32_e32 v101, 31, v100
	v_lshlrev_b64 v[100:101], 11, v[100:101]
	v_lshl_add_u64 v[100:101], s[8:9], 0, v[100:101]
	v_lshl_add_u64 v[100:101], v[100:101], 0, v[144:145]
	global_store_dwordx4 v[100:101], v[92:95], off sc0 sc1
	ds_read_b32 v92, v162 offset:2176
	v_cvt_f32_i32_e32 v99, v99
	v_cvt_f32_i32_e32 v98, v98
	v_cvt_f32_i32_e32 v95, v97
	v_cvt_f32_i32_e32 v94, v96
	v_cvt_f32_i32_e32 v89, v89
	v_cvt_f32_i32_e32 v88, v88
	s_waitcnt lgkmcnt(0)
	v_pk_mul_f32 v[100:101], v[134:135], v[92:93] op_sel_hi:[1,0]
	v_cvt_f32_i32_e32 v91, v91
	v_cvt_f32_i32_e32 v90, v90
	v_cvt_f32_i32_e32 v85, v85
	v_cvt_f32_i32_e32 v84, v84
	v_pk_mul_f32 v[96:97], v[132:133], v[92:93] op_sel_hi:[1,0]
	v_pk_fma_f32 v[98:99], v[100:101], v[98:99], v[138:139]
	v_cvt_f32_i32_e32 v77, v77
	v_cvt_f32_i32_e32 v79, v79
	v_cvt_f32_i32_e32 v78, v78
	v_cvt_f32_i32_e32 v76, v76
	v_pk_fma_f32 v[94:95], v[96:97], v[94:95], v[136:137]
	v_pk_mul_f32 v[96:97], v[98:99], v[98:99]
	v_pk_mul_f32 v[98:99], v[128:129], v[92:93] op_sel_hi:[1,0]
	v_pk_mul_f32 v[100:101], v[130:131], v[92:93] op_sel_hi:[1,0]
	v_pk_fma_f32 v[88:89], v[98:99], v[88:89], v[124:125]
	v_pk_mul_f32 v[98:99], v[140:141], v[92:93] op_sel_hi:[1,0]
	v_pk_fma_f32 v[90:91], v[100:101], v[90:91], v[126:127]
	v_pk_mul_f32 v[100:101], v[142:143], v[92:93] op_sel_hi:[1,0]
	v_pk_fma_f32 v[84:85], v[98:99], v[84:85], v[120:121]
	v_pk_mul_f32 v[98:99], v[112:113], v[92:93] op_sel_hi:[1,0]
	v_pk_mul_f32 v[92:93], v[114:115], v[92:93] op_sel_hi:[1,0]
	v_cvt_f32_i32_e32 v87, v87
	v_cvt_f32_i32_e32 v86, v86
	v_pk_fma_f32 v[78:79], v[92:93], v[78:79], v[118:119]
	v_pk_fma_f32 v[76:77], v[98:99], v[76:77], v[116:117]
	v_pk_mul_f32 v[94:95], v[94:95], v[94:95]
	v_pk_mul_f32 v[88:89], v[88:89], v[88:89]
	v_pk_mul_f32 v[84:85], v[84:85], v[84:85]
	v_pk_mul_f32 v[92:93], v[78:79], v[78:79]
	v_pk_mul_f32 v[98:99], v[76:77], v[76:77]
	v_pk_fma_f32 v[86:87], v[100:101], v[86:87], v[122:123]
	v_cvt_pk_fp8_f32 v76, v94, v95
	v_cvt_pk_fp8_f32 v77, v88, v89
	v_cvt_pk_fp8_f32 v78, v84, v85
	v_cvt_pk_fp8_f32 v79, v98, v99
	v_pk_mul_f32 v[90:91], v[90:91], v[90:91]
	v_pk_mul_f32 v[86:87], v[86:87], v[86:87]
	v_or_b32_e32 v84, 32, v146
	v_cvt_pk_fp8_f32 v76, v96, v97 op_sel:[0,0,1]
	v_cvt_pk_fp8_f32 v77, v90, v91 op_sel:[0,0,1]
	v_cvt_pk_fp8_f32 v78, v86, v87 op_sel:[0,0,1]
	v_cvt_pk_fp8_f32 v79, v92, v93 op_sel:[0,0,1]
	v_ashrrev_i32_e32 v85, 31, v84
	v_lshlrev_b64 v[84:85], 11, v[84:85]
	v_lshl_add_u64 v[84:85], s[8:9], 0, v[84:85]
	v_lshl_add_u64 v[84:85], v[84:85], 0, v[144:145]
	global_store_dwordx4 v[84:85], v[76:79], off sc0 sc1
	ds_read_b32 v76, v162 offset:2240
	v_cvt_f32_i32_e32 v83, v83
	v_cvt_f32_i32_e32 v82, v82
	v_cvt_f32_i32_e32 v79, v81
	v_cvt_f32_i32_e32 v78, v80
	v_cvt_f32_i32_e32 v73, v73
	v_cvt_f32_i32_e32 v72, v72
	s_waitcnt lgkmcnt(0)
	v_pk_mul_f32 v[84:85], v[134:135], v[76:77] op_sel_hi:[1,0]
	v_cvt_f32_i32_e32 v75, v75
	v_cvt_f32_i32_e32 v74, v74
	v_cvt_f32_i32_e32 v69, v69
	v_cvt_f32_i32_e32 v68, v68
	v_pk_mul_f32 v[80:81], v[132:133], v[76:77] op_sel_hi:[1,0]
	v_pk_fma_f32 v[82:83], v[84:85], v[82:83], v[138:139]
	v_cvt_f32_i32_e32 v65, v65
	v_cvt_f32_i32_e32 v67, v67
	v_cvt_f32_i32_e32 v66, v66
	v_cvt_f32_i32_e32 v64, v64
	v_pk_fma_f32 v[78:79], v[80:81], v[78:79], v[136:137]
	v_pk_mul_f32 v[80:81], v[82:83], v[82:83]
	v_pk_mul_f32 v[82:83], v[128:129], v[76:77] op_sel_hi:[1,0]
	v_pk_mul_f32 v[84:85], v[130:131], v[76:77] op_sel_hi:[1,0]
	v_pk_fma_f32 v[72:73], v[82:83], v[72:73], v[124:125]
	v_pk_mul_f32 v[82:83], v[140:141], v[76:77] op_sel_hi:[1,0]
	v_pk_fma_f32 v[74:75], v[84:85], v[74:75], v[126:127]
	v_pk_mul_f32 v[84:85], v[142:143], v[76:77] op_sel_hi:[1,0]
	v_pk_fma_f32 v[68:69], v[82:83], v[68:69], v[120:121]
	v_pk_mul_f32 v[82:83], v[112:113], v[76:77] op_sel_hi:[1,0]
	v_pk_mul_f32 v[76:77], v[114:115], v[76:77] op_sel_hi:[1,0]
	v_cvt_f32_i32_e32 v71, v71
	v_cvt_f32_i32_e32 v70, v70
	v_pk_fma_f32 v[66:67], v[76:77], v[66:67], v[118:119]
	v_pk_fma_f32 v[64:65], v[82:83], v[64:65], v[116:117]
	v_pk_mul_f32 v[78:79], v[78:79], v[78:79]
	v_pk_mul_f32 v[72:73], v[72:73], v[72:73]
	v_pk_mul_f32 v[68:69], v[68:69], v[68:69]
	v_pk_mul_f32 v[76:77], v[66:67], v[66:67]
	v_pk_mul_f32 v[82:83], v[64:65], v[64:65]
	v_pk_fma_f32 v[70:71], v[84:85], v[70:71], v[122:123]
	v_cvt_pk_fp8_f32 v64, v78, v79
	v_cvt_pk_fp8_f32 v65, v72, v73
	v_cvt_pk_fp8_f32 v66, v68, v69
	v_cvt_pk_fp8_f32 v67, v82, v83
	v_pk_mul_f32 v[74:75], v[74:75], v[74:75]
	v_pk_mul_f32 v[70:71], v[70:71], v[70:71]
	v_or_b32_e32 v68, 48, v146
	v_cvt_pk_fp8_f32 v64, v80, v81 op_sel:[0,0,1]
	v_cvt_pk_fp8_f32 v65, v74, v75 op_sel:[0,0,1]
	v_cvt_pk_fp8_f32 v66, v70, v71 op_sel:[0,0,1]
	v_cvt_pk_fp8_f32 v67, v76, v77 op_sel:[0,0,1]
	v_ashrrev_i32_e32 v69, 31, v68
	v_lshlrev_b64 v[68:69], 11, v[68:69]
	v_lshl_add_u64 v[68:69], s[8:9], 0, v[68:69]
	v_lshl_add_u64 v[68:69], v[68:69], 0, v[144:145]
	global_store_dwordx4 v[68:69], v[64:67], off sc0 sc1
	ds_read_b32 v64, v162 offset:2560
	v_cvt_f32_i32_e32 v61, v61
	v_cvt_f32_i32_e32 v60, v60
	v_cvt_f32_i32_e32 v63, v63
	v_cvt_f32_i32_e32 v62, v62
	v_cvt_f32_i32_e32 v57, v57
	v_cvt_f32_i32_e32 v56, v56
	v_cvt_f32_i32_e32 v59, v59
	v_cvt_f32_i32_e32 v58, v58
	v_cvt_f32_i32_e32 v49, v49
	v_cvt_f32_i32_e32 v48, v48
	s_waitcnt lgkmcnt(0)
	v_pk_mul_f32 v[66:67], v[132:133], v[64:65] op_sel_hi:[1,0]
	v_cvt_f32_i32_e32 v41, v41
	v_cvt_f32_i32_e32 v43, v43
	v_cvt_f32_i32_e32 v42, v42
	v_cvt_f32_i32_e32 v40, v40
	v_pk_mul_f32 v[68:69], v[134:135], v[64:65] op_sel_hi:[1,0]
	v_pk_fma_f32 v[60:61], v[66:67], v[60:61], v[136:137]
	v_pk_mul_f32 v[66:67], v[128:129], v[64:65] op_sel_hi:[1,0]
	v_pk_fma_f32 v[62:63], v[68:69], v[62:63], v[138:139]
	v_pk_mul_f32 v[68:69], v[130:131], v[64:65] op_sel_hi:[1,0]
	v_pk_fma_f32 v[56:57], v[66:67], v[56:57], v[124:125]
	v_pk_mul_f32 v[66:67], v[140:141], v[64:65] op_sel_hi:[1,0]
	v_pk_fma_f32 v[58:59], v[68:69], v[58:59], v[126:127]
	v_pk_mul_f32 v[68:69], v[142:143], v[64:65] op_sel_hi:[1,0]
	v_pk_fma_f32 v[48:49], v[66:67], v[48:49], v[120:121]
	v_pk_mul_f32 v[66:67], v[112:113], v[64:65] op_sel_hi:[1,0]
	v_pk_mul_f32 v[64:65], v[114:115], v[64:65] op_sel_hi:[1,0]
	v_cvt_f32_i32_e32 v51, v51
	v_cvt_f32_i32_e32 v50, v50
	v_pk_fma_f32 v[42:43], v[64:65], v[42:43], v[118:119]
	v_pk_fma_f32 v[40:41], v[66:67], v[40:41], v[116:117]
	v_pk_mul_f32 v[60:61], v[60:61], v[60:61]
	v_pk_mul_f32 v[56:57], v[56:57], v[56:57]
	v_pk_mul_f32 v[48:49], v[48:49], v[48:49]
	v_pk_mul_f32 v[64:65], v[42:43], v[42:43]
	v_pk_mul_f32 v[66:67], v[40:41], v[40:41]
	v_pk_fma_f32 v[50:51], v[68:69], v[50:51], v[122:123]
	v_cvt_pk_fp8_f32 v40, v60, v61
	v_cvt_pk_fp8_f32 v41, v56, v57
	v_cvt_pk_fp8_f32 v42, v48, v49
	v_cvt_pk_fp8_f32 v43, v66, v67
	v_pk_mul_f32 v[62:63], v[62:63], v[62:63]
	v_pk_mul_f32 v[58:59], v[58:59], v[58:59]
	v_pk_mul_f32 v[50:51], v[50:51], v[50:51]
	v_cvt_pk_fp8_f32 v40, v62, v63 op_sel:[0,0,1]
	v_cvt_pk_fp8_f32 v41, v58, v59 op_sel:[0,0,1]
	v_cvt_pk_fp8_f32 v42, v50, v51 op_sel:[0,0,1]
	v_cvt_pk_fp8_f32 v43, v64, v65 op_sel:[0,0,1]
	v_add_co_u32_e32 v48, vcc, s58, v148
	v_cvt_f32_i32_e32 v45, v45
	s_nop 0
	v_addc_co_u32_e32 v49, vcc, 0, v149, vcc
	global_store_dwordx4 v[48:49], v[40:43], off sc0 sc1
	ds_read_b32 v40, v162 offset:2624
	v_cvt_f32_i32_e32 v49, v55
	v_cvt_f32_i32_e32 v43, v53
	v_cvt_f32_i32_e32 v42, v52
	v_cvt_f32_i32_e32 v48, v54
	v_cvt_f32_i32_e32 v44, v44
	v_cvt_f32_i32_e32 v47, v47
	v_cvt_f32_i32_e32 v46, v46
	v_cvt_f32_i32_e32 v33, v33
	v_cvt_f32_i32_e32 v32, v32
	s_waitcnt lgkmcnt(0)
	v_pk_mul_f32 v[50:51], v[132:133], v[40:41] op_sel_hi:[1,0]
	v_cvt_f32_i32_e32 v25, v25
	v_cvt_f32_i32_e32 v27, v27
	v_cvt_f32_i32_e32 v26, v26
	v_cvt_f32_i32_e32 v24, v24
	v_pk_mul_f32 v[52:53], v[134:135], v[40:41] op_sel_hi:[1,0]
	v_pk_fma_f32 v[42:43], v[50:51], v[42:43], v[136:137]
	v_pk_mul_f32 v[50:51], v[128:129], v[40:41] op_sel_hi:[1,0]
	v_pk_fma_f32 v[48:49], v[52:53], v[48:49], v[138:139]
	v_pk_mul_f32 v[52:53], v[130:131], v[40:41] op_sel_hi:[1,0]
	v_pk_fma_f32 v[44:45], v[50:51], v[44:45], v[124:125]
	v_pk_mul_f32 v[50:51], v[140:141], v[40:41] op_sel_hi:[1,0]
	v_pk_fma_f32 v[46:47], v[52:53], v[46:47], v[126:127]
	v_pk_mul_f32 v[52:53], v[142:143], v[40:41] op_sel_hi:[1,0]
	v_pk_fma_f32 v[32:33], v[50:51], v[32:33], v[120:121]
	v_pk_mul_f32 v[50:51], v[112:113], v[40:41] op_sel_hi:[1,0]
	v_pk_mul_f32 v[40:41], v[114:115], v[40:41] op_sel_hi:[1,0]
	v_cvt_f32_i32_e32 v35, v35
	v_cvt_f32_i32_e32 v34, v34
	v_pk_fma_f32 v[26:27], v[40:41], v[26:27], v[118:119]
	v_pk_fma_f32 v[24:25], v[50:51], v[24:25], v[116:117]
	v_pk_mul_f32 v[42:43], v[42:43], v[42:43]
	v_pk_mul_f32 v[44:45], v[44:45], v[44:45]
	v_pk_mul_f32 v[32:33], v[32:33], v[32:33]
	v_pk_mul_f32 v[40:41], v[26:27], v[26:27]
	v_pk_mul_f32 v[50:51], v[24:25], v[24:25]
	v_pk_fma_f32 v[34:35], v[52:53], v[34:35], v[122:123]
	v_cvt_pk_fp8_f32 v24, v42, v43
	v_cvt_pk_fp8_f32 v25, v44, v45
	v_cvt_pk_fp8_f32 v26, v32, v33
	v_cvt_pk_fp8_f32 v27, v50, v51
	v_pk_mul_f32 v[48:49], v[48:49], v[48:49]
	v_pk_mul_f32 v[46:47], v[46:47], v[46:47]
	v_pk_mul_f32 v[34:35], v[34:35], v[34:35]
	v_cvt_pk_fp8_f32 v24, v48, v49 op_sel:[0,0,1]
	v_cvt_pk_fp8_f32 v25, v46, v47 op_sel:[0,0,1]
	v_cvt_pk_fp8_f32 v26, v34, v35 op_sel:[0,0,1]
	v_cvt_pk_fp8_f32 v27, v40, v41 op_sel:[0,0,1]
	v_add_co_u32_e32 v32, vcc, s59, v148
	v_cvt_f32_i32_e32 v29, v29
	s_nop 0
	v_addc_co_u32_e32 v33, vcc, 0, v149, vcc
	global_store_dwordx4 v[32:33], v[24:27], off sc0 sc1
	ds_read_b32 v24, v162 offset:2688
	v_cvt_f32_i32_e32 v33, v39
	v_cvt_f32_i32_e32 v27, v37
	v_cvt_f32_i32_e32 v26, v36
	v_cvt_f32_i32_e32 v32, v38
	v_cvt_f32_i32_e32 v28, v28
	v_cvt_f32_i32_e32 v31, v31
	v_cvt_f32_i32_e32 v30, v30
	v_cvt_f32_i32_e32 v17, v17
	v_cvt_f32_i32_e32 v16, v16
	s_waitcnt lgkmcnt(0)
	v_pk_mul_f32 v[34:35], v[132:133], v[24:25] op_sel_hi:[1,0]
	v_cvt_f32_i32_e32 v9, v9
	v_cvt_f32_i32_e32 v11, v11
	v_cvt_f32_i32_e32 v10, v10
	v_cvt_f32_i32_e32 v8, v8
	v_pk_mul_f32 v[36:37], v[134:135], v[24:25] op_sel_hi:[1,0]
	v_pk_fma_f32 v[26:27], v[34:35], v[26:27], v[136:137]
	v_pk_mul_f32 v[34:35], v[128:129], v[24:25] op_sel_hi:[1,0]
	v_pk_fma_f32 v[32:33], v[36:37], v[32:33], v[138:139]
	v_pk_mul_f32 v[36:37], v[130:131], v[24:25] op_sel_hi:[1,0]
	v_pk_fma_f32 v[28:29], v[34:35], v[28:29], v[124:125]
	v_pk_mul_f32 v[34:35], v[140:141], v[24:25] op_sel_hi:[1,0]
	v_pk_fma_f32 v[30:31], v[36:37], v[30:31], v[126:127]
	v_pk_mul_f32 v[36:37], v[142:143], v[24:25] op_sel_hi:[1,0]
	v_pk_fma_f32 v[16:17], v[34:35], v[16:17], v[120:121]
	v_pk_mul_f32 v[34:35], v[112:113], v[24:25] op_sel_hi:[1,0]
	v_pk_mul_f32 v[24:25], v[114:115], v[24:25] op_sel_hi:[1,0]
	v_cvt_f32_i32_e32 v19, v19
	v_cvt_f32_i32_e32 v18, v18
	v_pk_fma_f32 v[10:11], v[24:25], v[10:11], v[118:119]
	v_pk_fma_f32 v[8:9], v[34:35], v[8:9], v[116:117]
	v_pk_mul_f32 v[26:27], v[26:27], v[26:27]
	v_pk_mul_f32 v[28:29], v[28:29], v[28:29]
	v_pk_mul_f32 v[16:17], v[16:17], v[16:17]
	v_pk_mul_f32 v[24:25], v[10:11], v[10:11]
	v_pk_mul_f32 v[34:35], v[8:9], v[8:9]
	v_pk_fma_f32 v[18:19], v[36:37], v[18:19], v[122:123]
	v_cvt_pk_fp8_f32 v8, v26, v27
	v_cvt_pk_fp8_f32 v9, v28, v29
	v_cvt_pk_fp8_f32 v10, v16, v17
	v_cvt_pk_fp8_f32 v11, v34, v35
	v_pk_mul_f32 v[32:33], v[32:33], v[32:33]
	v_pk_mul_f32 v[30:31], v[30:31], v[30:31]
	v_pk_mul_f32 v[18:19], v[18:19], v[18:19]
	v_cvt_pk_fp8_f32 v8, v32, v33 op_sel:[0,0,1]
	v_cvt_pk_fp8_f32 v9, v30, v31 op_sel:[0,0,1]
	v_cvt_pk_fp8_f32 v10, v18, v19 op_sel:[0,0,1]
	v_cvt_pk_fp8_f32 v11, v24, v25 op_sel:[0,0,1]
	v_add_co_u32_e32 v16, vcc, s60, v148
	v_cvt_f32_i32_e32 v13, v13
	s_nop 0
	v_addc_co_u32_e32 v17, vcc, 0, v149, vcc
	global_store_dwordx4 v[16:17], v[8:11], off sc0 sc1
	ds_read_b32 v8, v162 offset:2752
	v_cvt_f32_i32_e32 v17, v23
	v_cvt_f32_i32_e32 v11, v21
	v_cvt_f32_i32_e32 v10, v20
	v_cvt_f32_i32_e32 v16, v22
	v_cvt_f32_i32_e32 v12, v12
	v_cvt_f32_i32_e32 v15, v15
	v_cvt_f32_i32_e32 v14, v14
	v_cvt_f32_i32_e32 v5, v5
	v_cvt_f32_i32_e32 v4, v4
	s_waitcnt lgkmcnt(0)
	v_pk_mul_f32 v[18:19], v[132:133], v[8:9] op_sel_hi:[1,0]
	v_cvt_f32_i32_e32 v1, v1
	v_cvt_f32_i32_e32 v3, v3
	v_cvt_f32_i32_e32 v2, v2
	v_cvt_f32_i32_e32 v0, v0
	v_pk_mul_f32 v[20:21], v[134:135], v[8:9] op_sel_hi:[1,0]
	v_pk_fma_f32 v[10:11], v[18:19], v[10:11], v[136:137]
	v_pk_mul_f32 v[18:19], v[128:129], v[8:9] op_sel_hi:[1,0]
	v_pk_fma_f32 v[16:17], v[20:21], v[16:17], v[138:139]
	v_pk_mul_f32 v[20:21], v[130:131], v[8:9] op_sel_hi:[1,0]
	v_pk_fma_f32 v[12:13], v[18:19], v[12:13], v[124:125]
	v_pk_mul_f32 v[18:19], v[140:141], v[8:9] op_sel_hi:[1,0]
	v_pk_fma_f32 v[14:15], v[20:21], v[14:15], v[126:127]
	v_pk_mul_f32 v[20:21], v[142:143], v[8:9] op_sel_hi:[1,0]
	v_pk_fma_f32 v[4:5], v[18:19], v[4:5], v[120:121]
	v_pk_mul_f32 v[18:19], v[112:113], v[8:9] op_sel_hi:[1,0]
	v_pk_mul_f32 v[8:9], v[114:115], v[8:9] op_sel_hi:[1,0]
	v_cvt_f32_i32_e32 v7, v7
	v_cvt_f32_i32_e32 v6, v6
	v_pk_fma_f32 v[2:3], v[8:9], v[2:3], v[118:119]
	v_pk_fma_f32 v[0:1], v[18:19], v[0:1], v[116:117]
	v_pk_mul_f32 v[10:11], v[10:11], v[10:11]
	v_pk_mul_f32 v[12:13], v[12:13], v[12:13]
	v_pk_mul_f32 v[4:5], v[4:5], v[4:5]
	v_pk_mul_f32 v[8:9], v[2:3], v[2:3]
	v_pk_mul_f32 v[18:19], v[0:1], v[0:1]
	v_pk_fma_f32 v[6:7], v[20:21], v[6:7], v[122:123]
	v_cvt_pk_fp8_f32 v0, v10, v11
	v_cvt_pk_fp8_f32 v1, v12, v13
	v_cvt_pk_fp8_f32 v2, v4, v5
	v_cvt_pk_fp8_f32 v3, v18, v19
	v_pk_mul_f32 v[16:17], v[16:17], v[16:17]
	v_pk_mul_f32 v[14:15], v[14:15], v[14:15]
	v_pk_mul_f32 v[6:7], v[6:7], v[6:7]
	v_cvt_pk_fp8_f32 v0, v16, v17 op_sel:[0,0,1]
	v_cvt_pk_fp8_f32 v1, v14, v15 op_sel:[0,0,1]
	v_cvt_pk_fp8_f32 v2, v6, v7 op_sel:[0,0,1]
	v_cvt_pk_fp8_f32 v3, v8, v9 op_sel:[0,0,1]
	v_add_co_u32_e32 v4, vcc, 0x58000, v148
	s_nop 1
	v_addc_co_u32_e32 v5, vcc, 0, v149, vcc
	global_store_dwordx4 v[4:5], v[0:3], off sc0 sc1
	s_branch .LBB2_25
